# LDS bank conflicts: weight-conversion tile [64][257] + 16 ds_write2_b32 (4-way conflicts) -> [64][256] XOR-swizzled by ((row>>3)&7)<<3, written with 8 ds_write_b128, transposed reads conflict-free
# speedup vs baseline: 1.0009x; 1.0009x over previous
.LBB0_218:
	v_add_u32_e32 v2, 0x800, v130
	s_lshr_b32 s0, s12, 8
	v_ashrrev_i32_e32 v41, 6, v2
	v_cvt_f32_u32_e32 v2, s0
	s_sub_i32 s13, 0, s0
	s_abs_i32 s9, s14
	s_ashr_i32 s8, s14, 31
	v_rcp_iflag_f32_e32 v2, v2
	v_add_u32_e32 v3, 0xa00, v130
	v_ashrrev_i32_e32 v42, 6, v3
	v_add_u32_e32 v3, 0xc00, v130
	v_mul_f32_e32 v2, 0x4f7ffffe, v2
	v_cvt_u32_f32_e32 v2, v2
	v_lshlrev_b32_e32 v1, 2, v130
	v_ashrrev_i32_e32 v43, 6, v3
	v_add_u32_e32 v3, 0xe00, v130
	v_readfirstlane_b32 s15, v2
	s_mul_i32 s13, s13, s15
	s_mul_hi_u32 s13, s15, s13
	s_add_i32 s15, s15, s13
	s_mul_hi_u32 s13, s9, s15
	s_mul_i32 s15, s13, s0
	s_sub_i32 s9, s9, s15
	s_add_i32 s15, s13, 1
	s_sub_i32 s16, s9, s0
	s_cmp_ge_u32 s9, s0
	s_cselect_b32 s13, s15, s13
	s_cselect_b32 s9, s16, s9
	s_add_i32 s15, s13, 1
	s_cmp_ge_u32 s9, s0
	s_cselect_b32 s9, s15, s13
	s_xor_b32 s9, s9, s8
	s_sub_i32 s13, s9, s8
	s_mul_i32 s0, s13, s0
	s_sub_i32 s0, s14, s0
	s_lshl_b32 s8, s0, 8
	s_ashr_i32 s9, s8, 31
	s_lshl_b64 s[14:15], s[8:9], 2
	s_add_u32 s10, s10, s14
	v_and_b32_e32 v36, 0xfc, v1
	v_ashrrev_i32_e32 v44, 6, v3
	s_addc_u32 s11, s11, s15
	s_lshl_b32 s16, s13, 6
	v_mov_b32_e32 v35, 0
	v_lshlrev_b32_e32 v34, 2, v36
	v_add_u32_e32 v4, s16, v44
	v_lshl_add_u64 v[2:3], s[10:11], 0, v[34:35]
	v_ashrrev_i32_e32 v7, 31, v4
	v_mad_u64_u32 v[4:5], s[10:11], v4, s12, 0
	v_mov_b32_e32 v6, v5
	v_mad_u64_u32 v[6:7], s[10:11], v7, s12, v[6:7]
	v_mov_b32_e32 v5, v6
	v_add_u32_e32 v6, s16, v43
	v_ashrrev_i32_e32 v9, 31, v6
	v_mad_u64_u32 v[6:7], s[10:11], v6, s12, 0
	v_mov_b32_e32 v8, v7
	v_mad_u64_u32 v[8:9], s[10:11], v9, s12, v[8:9]
	v_lshl_add_u64 v[4:5], v[4:5], 2, v[2:3]
	v_mov_b32_e32 v7, v8
	v_lshl_add_u64 v[6:7], v[6:7], 2, v[2:3]
	global_load_dwordx4 v[30:33], v[4:5], off
	global_load_dwordx4 v[26:29], v[6:7], off
	v_add_u32_e32 v4, s16, v42
	v_ashrrev_i32_e32 v7, 31, v4
	v_mad_u64_u32 v[4:5], s[10:11], v4, s12, 0
	v_mov_b32_e32 v6, v5
	v_mad_u64_u32 v[6:7], s[10:11], v7, s12, v[6:7]
	v_mov_b32_e32 v5, v6
	v_add_u32_e32 v6, s16, v41
	v_ashrrev_i32_e32 v9, 31, v6
	v_mad_u64_u32 v[6:7], s[10:11], v6, s12, 0
	v_mov_b32_e32 v8, v7
	v_add_u32_e32 v54, 0x600, v130
	v_mad_u64_u32 v[8:9], s[10:11], v9, s12, v[8:9]
	v_ashrrev_i32_e32 v40, 6, v54
	v_lshl_add_u64 v[4:5], v[4:5], 2, v[2:3]
	v_mov_b32_e32 v7, v8
	v_lshl_add_u64 v[6:7], v[6:7], 2, v[2:3]
	global_load_dwordx4 v[22:25], v[4:5], off
	global_load_dwordx4 v[18:21], v[6:7], off
	v_add_u32_e32 v4, s16, v40
	v_ashrrev_i32_e32 v7, 31, v4
	v_mad_u64_u32 v[4:5], s[10:11], v4, s12, 0
	v_add_u32_e32 v51, 0x400, v130
	v_mov_b32_e32 v6, v5
	v_ashrrev_i32_e32 v39, 6, v51
	v_mad_u64_u32 v[6:7], s[10:11], v7, s12, v[6:7]
	v_mov_b32_e32 v5, v6
	v_add_u32_e32 v6, s16, v39
	v_ashrrev_i32_e32 v9, 31, v6
	v_mad_u64_u32 v[6:7], s[10:11], v6, s12, 0
	v_mov_b32_e32 v8, v7
	v_add_u32_e32 v37, 0x200, v130
	v_mad_u64_u32 v[8:9], s[10:11], v9, s12, v[8:9]
	v_ashrrev_i32_e32 v38, 6, v37
	v_lshl_add_u64 v[4:5], v[4:5], 2, v[2:3]
	v_mov_b32_e32 v7, v8
	v_lshl_add_u64 v[6:7], v[6:7], 2, v[2:3]
	global_load_dwordx4 v[14:17], v[4:5], off
	global_load_dwordx4 v[10:13], v[6:7], off
	v_add_u32_e32 v4, s16, v38
	v_ashrrev_i32_e32 v7, 31, v4
	v_mad_u64_u32 v[4:5], s[10:11], v4, s12, 0
	v_mov_b32_e32 v6, v5
	v_ashrrev_i32_e32 v1, 6, v130
	v_mad_u64_u32 v[6:7], s[10:11], v7, s12, v[6:7]
	v_mov_b32_e32 v5, v6
	v_add_u32_e32 v6, s16, v1
	v_ashrrev_i32_e32 v9, 31, v6
	v_mad_u64_u32 v[6:7], s[10:11], v6, s12, 0
	v_mov_b32_e32 v8, v7
	v_mad_u64_u32 v[8:9], s[10:11], v9, s12, v[8:9]
	v_mov_b32_e32 v7, v8
	v_lshl_add_u64 v[4:5], v[4:5], 2, v[2:3]
	v_lshl_add_u64 v[2:3], v[6:7], 2, v[2:3]
	global_load_dwordx4 v[6:9], v[4:5], off
	s_nop 0
	global_load_dwordx4 v[2:5], v[2:3], off
	v_lshlrev_b32_e32 v45, 3, v130
	v_and_b32_e32 v66, 56, v45
	s_movk_i32 s0, 0x400
	v_mad_u32_u24 v55, v66, s0, 0
	v_mul_lo_u32 v57, v1, s0
	v_mul_lo_u32 v58, v38, s0
	v_mul_lo_u32 v59, v39, s0
	v_mul_lo_u32 v60, v40, s0
	v_mul_lo_u32 v61, v41, s0
	v_mul_lo_u32 v62, v42, s0
	v_mul_lo_u32 v63, v43, s0
	v_mul_lo_u32 v64, v44, s0
	s_add_u32 s0, s6, 0x1e940000
	s_addc_u32 s9, s7, 0
	s_add_u32 s12, s6, 0x16940000
	s_addc_u32 s13, s7, 0
	s_add_u32 s14, s6, 0x16140000
	s_addc_u32 s15, s7, 0
	s_add_u32 s30, s6, 0x15540000
	s_addc_u32 s31, s7, 0
	s_add_u32 s6, s6, 0x11f40000
	v_add_u32_e32 v34, 0, v34
	v_ashrrev_i32_e32 v45, 3, v130
	v_ashrrev_i32_e32 v48, 3, v37
	v_ashrrev_i32_e32 v51, 3, v51
	v_ashrrev_i32_e32 v54, 3, v54
	s_addc_u32 s7, s7, 0
	s_add_i32 s10, s33, s38
	s_mov_b32 s11, 0
	v_xor_b32_e32 v47, v45, v66
	v_lshl_add_u32 v46, v47, 2, v55
	v_and_b32_e32 v47, 15, v45
	v_xor_b32_e32 v50, v48, v66
	v_lshl_add_u32 v49, v50, 2, v55
	v_and_b32_e32 v50, 15, v48
	v_xor_b32_e32 v53, v51, v66
	v_lshl_add_u32 v52, v53, 2, v55
	v_and_b32_e32 v53, 15, v51
	v_xor_b32_e32 v56, v54, v66
	v_lshl_add_u32 v55, v56, 2, v55
	v_and_b32_e32 v56, 15, v54
	s_add_i32 s34, s10, 0xfffff5c0
	s_add_i32 s35, s10, 0xfffff6c0
	v_add_u32_e32 v57, v34, v57
	v_add_u32_e32 v58, v34, v58
	v_xor_b32_e32 v58, 32, v58
	v_add_u32_e32 v59, v34, v59
	v_xor_b32_e32 v59, 64, v59
	v_add_u32_e32 v60, v34, v60
	v_xor_b32_e32 v60, 96, v60
	v_add_u32_e32 v61, v34, v61
	v_xor_b32_e32 v61, 128, v61
	v_add_u32_e32 v62, v34, v62
	v_xor_b32_e32 v62, 160, v62
	v_add_u32_e32 v63, v34, v63
	v_xor_b32_e32 v63, 192, v63
	v_add_u32_e32 v64, v34, v64
	v_xor_b32_e32 v64, 224, v64
	v_lshlrev_b32_e32 v34, 2, v36
	v_lshlrev_b32_e32 v36, 1, v66
	s_movk_i32 s36, 0x7fff
	v_mov_b32_e32 v65, 1
	s_mov_b32 s26, s17
	s_mov_b32 s27, s29
	s_mov_b64 s[20:21], s[2:3]
	s_branch .LBB0_222

.LBB0_221:
	s_add_i32 s28, s28, -1
	s_cmp_eq_u32 s17, 0
	v_add_u32_e32 v66, s8, v45
	v_lshlrev_b32_e32 v37, 1, v66
	s_cselect_b64 vcc, -1, 0
	s_ashr_i32 s17, s16, 31
	v_and_b32_e32 v37, 0xffffffe0, v37
	s_lshl_b64 s[16:17], s[16:17], 1
	v_add3_u32 v67, s1, v47, v37
	s_add_u32 s2, s2, s16
	s_addc_u32 s3, s3, s17
	v_mov_b32_e32 v37, v35
	v_cndmask_b32_e32 v66, v67, v66, vcc
	v_lshl_add_u64 v[70:71], s[2:3], 0, v[36:37]
	v_ashrrev_i32_e32 v69, 31, v66
	v_mad_u64_u32 v[66:67], s[2:3], v66, s29, 0
	v_mov_b32_e32 v68, v67
	ds_read_b32 v37, v46
	ds_read_b32 v74, v46 offset:1024
	ds_read_b32 v75, v46 offset:2048
	ds_read_b32 v76, v46 offset:3072
	ds_read_b32 v77, v46 offset:4096
	ds_read_b32 v78, v46 offset:5120
	ds_read_b32 v79, v46 offset:6144
	ds_read_b32 v80, v46 offset:7168
	v_mad_u64_u32 v[68:69], s[2:3], v69, s29, v[68:69]
	v_mov_b32_e32 v67, v68
	v_lshl_add_u64 v[72:73], v[66:67], 1, v[70:71]
	s_waitcnt lgkmcnt(7)
	v_and_b32_sdwa v67, v37, v65 dst_sel:DWORD dst_unused:UNUSED_PAD src0_sel:WORD_1 src1_sel:DWORD
	v_add3_u32 v37, v37, v67, s36
	s_waitcnt lgkmcnt(4)
	v_and_b32_sdwa v67, v76, v65 dst_sel:DWORD dst_unused:UNUSED_PAD src0_sel:WORD_1 src1_sel:DWORD
	v_and_b32_sdwa v68, v74, v65 dst_sel:DWORD dst_unused:UNUSED_PAD src0_sel:WORD_1 src1_sel:DWORD
	v_and_b32_sdwa v66, v75, v65 dst_sel:DWORD dst_unused:UNUSED_PAD src0_sel:WORD_1 src1_sel:DWORD
	v_add3_u32 v67, v76, v67, s36
	v_add3_u32 v68, v74, v68, s36
	v_add3_u32 v66, v75, v66, s36
	v_and_b32_e32 v67, 0xffff0000, v67
	v_and_b32_e32 v68, 0xffff0000, v68
	s_waitcnt lgkmcnt(0)
	v_and_b32_sdwa v69, v80, v65 dst_sel:DWORD dst_unused:UNUSED_PAD src0_sel:WORD_1 src1_sel:DWORD
	v_and_b32_sdwa v74, v78, v65 dst_sel:DWORD dst_unused:UNUSED_PAD src0_sel:WORD_1 src1_sel:DWORD
	v_or_b32_sdwa v67, v67, v66 dst_sel:DWORD dst_unused:UNUSED_PAD src0_sel:DWORD src1_sel:WORD_1
	v_or_b32_sdwa v66, v68, v37 dst_sel:DWORD dst_unused:UNUSED_PAD src0_sel:DWORD src1_sel:WORD_1
	v_and_b32_sdwa v37, v79, v65 dst_sel:DWORD dst_unused:UNUSED_PAD src0_sel:WORD_1 src1_sel:DWORD
	v_and_b32_sdwa v68, v77, v65 dst_sel:DWORD dst_unused:UNUSED_PAD src0_sel:WORD_1 src1_sel:DWORD
	v_add3_u32 v69, v80, v69, s36
	v_add3_u32 v74, v78, v74, s36
	v_add3_u32 v68, v77, v68, s36
	v_add3_u32 v37, v79, v37, s36
	v_and_b32_e32 v69, 0xffff0000, v69
	v_and_b32_e32 v74, 0xffff0000, v74
	v_or_b32_sdwa v69, v69, v37 dst_sel:DWORD dst_unused:UNUSED_PAD src0_sel:DWORD src1_sel:WORD_1
	v_or_b32_sdwa v68, v74, v68 dst_sel:DWORD dst_unused:UNUSED_PAD src0_sel:DWORD src1_sel:WORD_1
	global_store_dwordx4 v[72:73], v[66:69], off
	ds_read_b32 v37, v49
	ds_read_b32 v74, v49 offset:1024
	ds_read_b32 v75, v49 offset:2048
	ds_read_b32 v76, v49 offset:3072
	ds_read_b32 v77, v49 offset:4096
	ds_read_b32 v78, v49 offset:5120
	ds_read_b32 v79, v49 offset:6144
	ds_read_b32 v80, v49 offset:7168
	v_add_u32_e32 v66, s8, v48
	v_lshlrev_b32_e32 v67, 1, v66
	v_and_b32_e32 v67, 0xffffffe0, v67
	v_add3_u32 v67, s1, v50, v67
	v_cndmask_b32_e32 v66, v67, v66, vcc
	v_ashrrev_i32_e32 v69, 31, v66
	v_mad_u64_u32 v[66:67], s[2:3], v66, s29, 0
	v_mov_b32_e32 v68, v67
	v_mad_u64_u32 v[68:69], s[2:3], v69, s29, v[68:69]
	v_mov_b32_e32 v67, v68
	v_lshl_add_u64 v[72:73], v[66:67], 1, v[70:71]
	s_waitcnt lgkmcnt(7)
	v_and_b32_sdwa v67, v37, v65 dst_sel:DWORD dst_unused:UNUSED_PAD src0_sel:WORD_1 src1_sel:DWORD
	v_add3_u32 v37, v37, v67, s36
	s_waitcnt lgkmcnt(4)
	v_and_b32_sdwa v67, v76, v65 dst_sel:DWORD dst_unused:UNUSED_PAD src0_sel:WORD_1 src1_sel:DWORD
	v_and_b32_sdwa v68, v74, v65 dst_sel:DWORD dst_unused:UNUSED_PAD src0_sel:WORD_1 src1_sel:DWORD
	v_and_b32_sdwa v66, v75, v65 dst_sel:DWORD dst_unused:UNUSED_PAD src0_sel:WORD_1 src1_sel:DWORD
	v_add3_u32 v67, v76, v67, s36
	v_add3_u32 v68, v74, v68, s36
	v_add3_u32 v66, v75, v66, s36
	v_and_b32_e32 v67, 0xffff0000, v67
	v_and_b32_e32 v68, 0xffff0000, v68
	s_waitcnt lgkmcnt(0)
	v_and_b32_sdwa v69, v80, v65 dst_sel:DWORD dst_unused:UNUSED_PAD src0_sel:WORD_1 src1_sel:DWORD
	v_and_b32_sdwa v74, v78, v65 dst_sel:DWORD dst_unused:UNUSED_PAD src0_sel:WORD_1 src1_sel:DWORD
	v_or_b32_sdwa v67, v67, v66 dst_sel:DWORD dst_unused:UNUSED_PAD src0_sel:DWORD src1_sel:WORD_1
	v_or_b32_sdwa v66, v68, v37 dst_sel:DWORD dst_unused:UNUSED_PAD src0_sel:DWORD src1_sel:WORD_1
	v_and_b32_sdwa v37, v79, v65 dst_sel:DWORD dst_unused:UNUSED_PAD src0_sel:WORD_1 src1_sel:DWORD
	v_and_b32_sdwa v68, v77, v65 dst_sel:DWORD dst_unused:UNUSED_PAD src0_sel:WORD_1 src1_sel:DWORD
	v_add3_u32 v69, v80, v69, s36
	v_add3_u32 v74, v78, v74, s36
	v_add3_u32 v68, v77, v68, s36
	v_add3_u32 v37, v79, v37, s36
	v_and_b32_e32 v69, 0xffff0000, v69
	v_and_b32_e32 v74, 0xffff0000, v74
	v_or_b32_sdwa v69, v69, v37 dst_sel:DWORD dst_unused:UNUSED_PAD src0_sel:DWORD src1_sel:WORD_1
	v_or_b32_sdwa v68, v74, v68 dst_sel:DWORD dst_unused:UNUSED_PAD src0_sel:DWORD src1_sel:WORD_1
	global_store_dwordx4 v[72:73], v[66:69], off
	ds_read_b32 v37, v52
	ds_read_b32 v74, v52 offset:1024
	ds_read_b32 v75, v52 offset:2048
	ds_read_b32 v76, v52 offset:3072
	ds_read_b32 v77, v52 offset:4096
	ds_read_b32 v78, v52 offset:5120
	ds_read_b32 v79, v52 offset:6144
	ds_read_b32 v80, v52 offset:7168
	v_add_u32_e32 v66, s8, v51
	v_lshlrev_b32_e32 v67, 1, v66
	v_and_b32_e32 v67, 0xffffffe0, v67
	v_add3_u32 v67, s1, v53, v67
	v_cndmask_b32_e32 v66, v67, v66, vcc
	v_ashrrev_i32_e32 v69, 31, v66
	v_mad_u64_u32 v[66:67], s[2:3], v66, s29, 0
	v_mov_b32_e32 v68, v67
	v_mad_u64_u32 v[68:69], s[2:3], v69, s29, v[68:69]
	v_mov_b32_e32 v67, v68
	v_lshl_add_u64 v[72:73], v[66:67], 1, v[70:71]
	s_waitcnt lgkmcnt(7)
	v_and_b32_sdwa v67, v37, v65 dst_sel:DWORD dst_unused:UNUSED_PAD src0_sel:WORD_1 src1_sel:DWORD
	v_add3_u32 v37, v37, v67, s36
	s_waitcnt lgkmcnt(4)
	v_and_b32_sdwa v67, v76, v65 dst_sel:DWORD dst_unused:UNUSED_PAD src0_sel:WORD_1 src1_sel:DWORD
	v_and_b32_sdwa v68, v74, v65 dst_sel:DWORD dst_unused:UNUSED_PAD src0_sel:WORD_1 src1_sel:DWORD
	v_and_b32_sdwa v66, v75, v65 dst_sel:DWORD dst_unused:UNUSED_PAD src0_sel:WORD_1 src1_sel:DWORD
	v_add3_u32 v67, v76, v67, s36
	v_add3_u32 v68, v74, v68, s36
	v_add3_u32 v66, v75, v66, s36
	v_and_b32_e32 v67, 0xffff0000, v67
	v_and_b32_e32 v68, 0xffff0000, v68
	s_waitcnt lgkmcnt(0)
	v_and_b32_sdwa v69, v80, v65 dst_sel:DWORD dst_unused:UNUSED_PAD src0_sel:WORD_1 src1_sel:DWORD
	v_and_b32_sdwa v74, v78, v65 dst_sel:DWORD dst_unused:UNUSED_PAD src0_sel:WORD_1 src1_sel:DWORD
	v_or_b32_sdwa v67, v67, v66 dst_sel:DWORD dst_unused:UNUSED_PAD src0_sel:DWORD src1_sel:WORD_1
	v_or_b32_sdwa v66, v68, v37 dst_sel:DWORD dst_unused:UNUSED_PAD src0_sel:DWORD src1_sel:WORD_1
	v_and_b32_sdwa v37, v79, v65 dst_sel:DWORD dst_unused:UNUSED_PAD src0_sel:WORD_1 src1_sel:DWORD
	v_and_b32_sdwa v68, v77, v65 dst_sel:DWORD dst_unused:UNUSED_PAD src0_sel:WORD_1 src1_sel:DWORD
	v_add3_u32 v69, v80, v69, s36
	v_add3_u32 v74, v78, v74, s36
	v_add3_u32 v68, v77, v68, s36
	v_add3_u32 v37, v79, v37, s36
	v_and_b32_e32 v69, 0xffff0000, v69
	v_and_b32_e32 v74, 0xffff0000, v74
	v_or_b32_sdwa v69, v69, v37 dst_sel:DWORD dst_unused:UNUSED_PAD src0_sel:DWORD src1_sel:WORD_1
	v_or_b32_sdwa v68, v74, v68 dst_sel:DWORD dst_unused:UNUSED_PAD src0_sel:DWORD src1_sel:WORD_1
	global_store_dwordx4 v[72:73], v[66:69], off
	ds_read_b32 v37, v55
	ds_read_b32 v72, v55 offset:1024
	ds_read_b32 v73, v55 offset:2048
	ds_read_b32 v74, v55 offset:3072
	ds_read_b32 v75, v55 offset:4096
	ds_read_b32 v76, v55 offset:5120
	ds_read_b32 v77, v55 offset:6144
	ds_read_b32 v78, v55 offset:7168
	v_add_u32_e32 v66, s8, v54
	v_lshlrev_b32_e32 v67, 1, v66
	v_and_b32_e32 v67, 0xffffffe0, v67
	v_add3_u32 v67, s1, v56, v67
	v_cndmask_b32_e32 v66, v67, v66, vcc
	v_ashrrev_i32_e32 v69, 31, v66
	v_mad_u64_u32 v[66:67], s[2:3], v66, s29, 0
	v_mov_b32_e32 v68, v67
	v_mad_u64_u32 v[68:69], s[2:3], v69, s29, v[68:69]
	v_mov_b32_e32 v67, v68
	v_lshl_add_u64 v[70:71], v[66:67], 1, v[70:71]
	s_waitcnt lgkmcnt(7)
	v_and_b32_sdwa v67, v37, v65 dst_sel:DWORD dst_unused:UNUSED_PAD src0_sel:WORD_1 src1_sel:DWORD
	v_add3_u32 v37, v37, v67, s36
	s_waitcnt lgkmcnt(4)
	v_and_b32_sdwa v67, v74, v65 dst_sel:DWORD dst_unused:UNUSED_PAD src0_sel:WORD_1 src1_sel:DWORD
	v_and_b32_sdwa v68, v72, v65 dst_sel:DWORD dst_unused:UNUSED_PAD src0_sel:WORD_1 src1_sel:DWORD
	v_and_b32_sdwa v66, v73, v65 dst_sel:DWORD dst_unused:UNUSED_PAD src0_sel:WORD_1 src1_sel:DWORD
	v_add3_u32 v67, v74, v67, s36
	v_add3_u32 v68, v72, v68, s36
	v_add3_u32 v66, v73, v66, s36
	v_and_b32_e32 v67, 0xffff0000, v67
	v_and_b32_e32 v68, 0xffff0000, v68
	s_waitcnt lgkmcnt(0)
	v_and_b32_sdwa v69, v78, v65 dst_sel:DWORD dst_unused:UNUSED_PAD src0_sel:WORD_1 src1_sel:DWORD
	v_and_b32_sdwa v72, v76, v65 dst_sel:DWORD dst_unused:UNUSED_PAD src0_sel:WORD_1 src1_sel:DWORD
	v_or_b32_sdwa v67, v67, v66 dst_sel:DWORD dst_unused:UNUSED_PAD src0_sel:DWORD src1_sel:WORD_1
	v_or_b32_sdwa v66, v68, v37 dst_sel:DWORD dst_unused:UNUSED_PAD src0_sel:DWORD src1_sel:WORD_1
	v_and_b32_sdwa v37, v77, v65 dst_sel:DWORD dst_unused:UNUSED_PAD src0_sel:WORD_1 src1_sel:DWORD
	v_and_b32_sdwa v68, v75, v65 dst_sel:DWORD dst_unused:UNUSED_PAD src0_sel:WORD_1 src1_sel:DWORD
	v_add3_u32 v69, v78, v69, s36
	v_add3_u32 v72, v76, v72, s36
	v_add3_u32 v68, v75, v68, s36
	v_add3_u32 v37, v77, v37, s36
	v_and_b32_e32 v69, 0xffff0000, v69
	v_and_b32_e32 v72, 0xffff0000, v72
	v_or_b32_sdwa v69, v69, v37 dst_sel:DWORD dst_unused:UNUSED_PAD src0_sel:DWORD src1_sel:WORD_1
	v_or_b32_sdwa v68, v72, v68 dst_sel:DWORD dst_unused:UNUSED_PAD src0_sel:DWORD src1_sel:WORD_1
	s_add_i32 s34, s34, s38
	s_add_i32 s35, s35, s38
	s_andn2_b64 vcc, exec, s[18:19]
	s_mov_b32 s1, s37
	s_mov_b32 s17, s26
	s_mov_b32 s8, s22
	s_mov_b32 s16, s10
	s_mov_b32 s29, s27
	s_mov_b64 s[2:3], s[20:21]
	global_store_dwordx4 v[70:71], v[66:69], off
	s_barrier
	s_cbranch_vccz .LBB0_240
.LBB0_222:
	s_add_i32 s33, s33, s38
	s_cmp_lt_u32 s28, 2
	s_cselect_b64 s[18:19], -1, 0
	s_and_b64 vcc, exec, s[18:19]
	s_mov_b32 s37, s1
	s_mov_b32 s22, s8
	s_mov_b32 s10, s16
	s_waitcnt vmcnt(0)
	ds_write_b128 v57, v[2:5]
	ds_write_b128 v58, v[6:9]
	ds_write_b128 v59, v[10:13]
	ds_write_b128 v60, v[14:17]
	ds_write_b128 v61, v[18:21]
	ds_write_b128 v62, v[22:25]
	ds_write_b128 v63, v[26:29]
	ds_write_b128 v64, v[30:33]
	s_waitcnt lgkmcnt(0)
	s_barrier
	s_cbranch_vccnz .LBB0_221
	s_add_i32 s10, s34, 0xa40
	s_cmpk_lt_i32 s10, 0x6c0
	s_cbranch_scc1 .LBB0_219
	s_cmpk_gt_u32 s10, 0x83f
	s_mov_b64 s[22:23], -1
	s_cbranch_scc0 .LBB0_237
	s_cmpk_gt_u32 s10, 0x93f
	s_cbranch_scc0 .LBB0_234
	s_mul_hi_u32 s10, s35, 0xaaaaaaab
	s_lshr_b32 s10, s10, 8
	s_mul_i32 s20, s10, 0xfffffe80
	s_add_i32 s10, s34, 0x100
	s_mul_hi_u32 s10, s10, 0xaaaaaaab
	s_lshr_b32 s10, s10, 8
	s_mul_i32 s21, s10, 0xfffffe80
	s_add_i32 s41, s33, s21
	s_add_i32 s40, s34, s20
	s_addk_i32 s41, 0xf6c0
	s_add_i32 s42, s40, 0x100
	s_cmpk_gt_i32 s42, 0x7f
	s_cbranch_scc0 .LBB0_231
	s_lshl_b64 s[22:23], s[10:11], 23
	s_cmpk_gt_u32 s42, 0xff
	s_mov_b64 s[26:27], -1
	s_cbranch_scc0 .LBB0_229
	s_add_u32 s24, s88, s22
	s_addc_u32 s25, s89, s23
	s_lshl_b64 s[20:21], s[10:11], 22
	s_add_u32 s20, s0, s20
	s_addc_u32 s21, s9, s21
	s_mov_b64 s[26:27], 0

.LBB0_1942:
	s_waitcnt vmcnt(11)
	v_add_u32_e32 v2, 0x800, v34
	s_lshr_b32 s4, s8, 8
	v_ashrrev_i32_e32 v42, 6, v2
	v_cvt_f32_u32_e32 v2, s4
	s_sub_i32 s11, 0, s4
	s_abs_i32 s10, s9
	s_ashr_i32 s5, s9, 31
	v_rcp_iflag_f32_e32 v2, v2
	v_add_u32_e32 v3, 0xa00, v34
	v_ashrrev_i32_e32 v43, 6, v3
	v_add_u32_e32 v3, 0xc00, v34
	v_mul_f32_e32 v2, 0x4f7ffffe, v2
	v_cvt_u32_f32_e32 v2, v2
	v_lshlrev_b32_e32 v1, 2, v34
	v_ashrrev_i32_e32 v44, 6, v3
	v_add_u32_e32 v3, 0xe00, v34
	v_readfirstlane_b32 s12, v2
	s_mul_i32 s11, s11, s12
	s_mul_hi_u32 s11, s12, s11
	s_add_i32 s12, s12, s11
	s_mul_hi_u32 s11, s10, s12
	s_mul_i32 s12, s11, s4
	s_sub_i32 s10, s10, s12
	s_add_i32 s12, s11, 1
	s_sub_i32 s13, s10, s4
	s_cmp_ge_u32 s10, s4
	s_cselect_b32 s11, s12, s11
	s_cselect_b32 s10, s13, s10
	s_add_i32 s12, s11, 1
	s_cmp_ge_u32 s10, s4
	s_cselect_b32 s10, s12, s11
	s_xor_b32 s10, s10, s5
	s_sub_i32 s12, s10, s5
	s_mul_i32 s4, s12, s4
	s_sub_i32 s4, s9, s4
	s_lshl_b32 s4, s4, 8
	s_ashr_i32 s5, s4, 31
	s_lshl_b64 s[10:11], s[4:5], 2
	s_add_u32 s6, s6, s10
	v_and_b32_e32 v38, 0xfc, v1
	v_ashrrev_i32_e32 v45, 6, v3
	s_addc_u32 s7, s7, s11
	s_lshl_b32 s14, s12, 6
	v_mov_b32_e32 v37, 0
	v_lshlrev_b32_e32 v36, 2, v38
	v_add_u32_e32 v4, s14, v45
	v_lshl_add_u64 v[2:3], s[6:7], 0, v[36:37]
	s_waitcnt vmcnt(10)
	v_ashrrev_i32_e32 v7, 31, v4
	v_mad_u64_u32 v[4:5], s[6:7], v4, s8, 0
	v_mov_b32_e32 v6, v5
	v_mad_u64_u32 v[6:7], s[6:7], v7, s8, v[6:7]
	v_mov_b32_e32 v5, v6
	v_add_u32_e32 v6, s14, v44
	v_ashrrev_i32_e32 v9, 31, v6
	v_mad_u64_u32 v[6:7], s[6:7], v6, s8, 0
	v_mov_b32_e32 v8, v7
	v_mad_u64_u32 v[8:9], s[6:7], v9, s8, v[8:9]
	v_lshl_add_u64 v[4:5], v[4:5], 2, v[2:3]
	v_mov_b32_e32 v7, v8
	v_lshl_add_u64 v[6:7], v[6:7], 2, v[2:3]
	global_load_dwordx4 v[30:33], v[4:5], off
	global_load_dwordx4 v[26:29], v[6:7], off
	v_add_u32_e32 v4, s14, v43
	v_ashrrev_i32_e32 v7, 31, v4
	v_mad_u64_u32 v[4:5], s[6:7], v4, s8, 0
	v_mov_b32_e32 v6, v5
	v_mad_u64_u32 v[6:7], s[6:7], v7, s8, v[6:7]
	v_mov_b32_e32 v5, v6
	v_add_u32_e32 v6, s14, v42
	v_ashrrev_i32_e32 v9, 31, v6
	v_mad_u64_u32 v[6:7], s[6:7], v6, s8, 0
	v_mov_b32_e32 v8, v7
	v_add_u32_e32 v55, 0x600, v34
	v_mad_u64_u32 v[8:9], s[6:7], v9, s8, v[8:9]
	v_ashrrev_i32_e32 v41, 6, v55
	v_lshl_add_u64 v[4:5], v[4:5], 2, v[2:3]
	v_mov_b32_e32 v7, v8
	v_lshl_add_u64 v[6:7], v[6:7], 2, v[2:3]
	global_load_dwordx4 v[22:25], v[4:5], off
	global_load_dwordx4 v[18:21], v[6:7], off
	v_add_u32_e32 v4, s14, v41
	v_ashrrev_i32_e32 v7, 31, v4
	v_mad_u64_u32 v[4:5], s[6:7], v4, s8, 0
	v_add_u32_e32 v52, 0x400, v34
	v_mov_b32_e32 v6, v5
	v_ashrrev_i32_e32 v40, 6, v52
	v_mad_u64_u32 v[6:7], s[6:7], v7, s8, v[6:7]
	v_mov_b32_e32 v5, v6
	v_add_u32_e32 v6, s14, v40
	v_ashrrev_i32_e32 v9, 31, v6
	v_mad_u64_u32 v[6:7], s[6:7], v6, s8, 0
	v_mov_b32_e32 v8, v7
	v_add_u32_e32 v39, 0x200, v34
	v_mad_u64_u32 v[8:9], s[6:7], v9, s8, v[8:9]
	v_ashrrev_i32_e32 v35, 6, v39
	v_lshl_add_u64 v[4:5], v[4:5], 2, v[2:3]
	v_mov_b32_e32 v7, v8
	v_lshl_add_u64 v[6:7], v[6:7], 2, v[2:3]
	global_load_dwordx4 v[14:17], v[4:5], off
	global_load_dwordx4 v[10:13], v[6:7], off
	v_add_u32_e32 v4, s14, v35
	v_ashrrev_i32_e32 v7, 31, v4
	v_mad_u64_u32 v[4:5], s[6:7], v4, s8, 0
	v_mov_b32_e32 v6, v5
	v_ashrrev_i32_e32 v1, 6, v34
	v_mad_u64_u32 v[6:7], s[6:7], v7, s8, v[6:7]
	v_mov_b32_e32 v5, v6
	v_add_u32_e32 v6, s14, v1
	v_ashrrev_i32_e32 v9, 31, v6
	v_mad_u64_u32 v[6:7], s[6:7], v6, s8, 0
	v_mov_b32_e32 v8, v7
	v_mad_u64_u32 v[8:9], s[6:7], v9, s8, v[8:9]
	v_mov_b32_e32 v7, v8
	v_lshl_add_u64 v[4:5], v[4:5], 2, v[2:3]
	v_lshl_add_u64 v[2:3], v[6:7], 2, v[2:3]
	global_load_dwordx4 v[6:9], v[4:5], off
	s_nop 0
	global_load_dwordx4 v[2:5], v[2:3], off
	v_lshlrev_b32_e32 v46, 3, v34
	v_and_b32_e32 v66, 56, v46
	s_movk_i32 s5, 0x400
	v_readlane_b32 s12, v251, 60
	v_mad_u32_u24 v56, v66, s5, 0
	v_mul_lo_u32 v58, v1, s5
	v_mul_lo_u32 v59, v35, s5
	v_mul_lo_u32 v60, v40, s5
	v_mul_lo_u32 v61, v41, s5
	v_mul_lo_u32 v62, v42, s5
	v_mul_lo_u32 v63, v43, s5
	v_mul_lo_u32 v64, v44, s5
	v_mul_lo_u32 v65, v45, s5
	v_readlane_b32 s13, v251, 61
	s_add_u32 s5, s12, 0x1e940000
	s_addc_u32 s26, s13, 0
	s_add_u32 s8, s12, 0x16940000
	s_addc_u32 s9, s13, 0
	s_add_u32 s10, s12, 0x16140000
	s_addc_u32 s11, s13, 0
	s_add_u32 s27, s12, 0x15540000
	s_addc_u32 s28, s13, 0
	v_add_u32_e32 v36, 0, v36
	v_ashrrev_i32_e32 v46, 3, v34
	v_ashrrev_i32_e32 v49, 3, v39
	v_ashrrev_i32_e32 v52, 3, v52
	v_ashrrev_i32_e32 v55, 3, v55
	s_add_u32 s12, s12, 0x11f40000
	s_mov_b32 s7, 0
	v_xor_b32_e32 v48, v46, v66
	v_lshl_add_u32 v47, v48, 2, v56
	v_and_b32_e32 v48, 15, v46
	v_xor_b32_e32 v51, v49, v66
	v_lshl_add_u32 v50, v51, 2, v56
	v_and_b32_e32 v51, 15, v49
	v_xor_b32_e32 v54, v52, v66
	v_lshl_add_u32 v53, v54, 2, v56
	v_and_b32_e32 v54, 15, v52
	v_xor_b32_e32 v57, v55, v66
	v_lshl_add_u32 v56, v57, 2, v56
	v_and_b32_e32 v57, 15, v55
	s_addc_u32 s13, s13, 0
	s_add_i32 s29, s16, 0x15e1
	s_mov_b32 s30, 17
	v_add_u32_e32 v58, v36, v58
	v_add_u32_e32 v59, v36, v59
	v_xor_b32_e32 v59, 32, v59
	v_add_u32_e32 v60, v36, v60
	v_xor_b32_e32 v60, 64, v60
	v_add_u32_e32 v61, v36, v61
	v_xor_b32_e32 v61, 96, v61
	v_add_u32_e32 v62, v36, v62
	v_xor_b32_e32 v62, 128, v62
	v_add_u32_e32 v63, v36, v63
	v_xor_b32_e32 v63, 160, v63
	v_add_u32_e32 v64, v36, v64
	v_xor_b32_e32 v64, 192, v64
	v_add_u32_e32 v65, v36, v65
	v_xor_b32_e32 v65, 224, v65
	v_lshlrev_b32_e32 v36, 2, v38
	v_lshlrev_b32_e32 v38, 1, v66
	s_movk_i32 s31, 0x7fff
	v_mov_b32_e32 v66, 1
	s_mov_b32 s24, s15
	s_mov_b32 s25, s0
	s_mov_b64 s[18:19], s[2:3]
	v_readlane_b32 s42, v251, 58
	v_readlane_b32 s43, v251, 59
	s_branch .LBB0_1946

.LBB0_1945:
	s_add_i32 s30, s30, -1
	s_cmp_eq_u32 s15, 0
	v_add_u32_e32 v67, s4, v46
	v_lshlrev_b32_e32 v39, 1, v67
	s_cselect_b64 vcc, -1, 0
	s_ashr_i32 s15, s14, 31
	v_and_b32_e32 v39, 0xffffffe0, v39
	s_lshl_b64 s[14:15], s[14:15], 1
	v_add3_u32 v68, s1, v48, v39
	s_add_u32 s2, s2, s14
	s_addc_u32 s3, s3, s15
	v_mov_b32_e32 v39, v37
	v_cndmask_b32_e32 v67, v68, v67, vcc
	v_lshl_add_u64 v[72:73], s[2:3], 0, v[38:39]
	v_mad_u64_u32 v[68:69], s[2:3], v67, s0, 0
	v_ashrrev_i32_e32 v71, 31, v67
	v_mov_b32_e32 v70, v69
	v_mad_u64_u32 v[70:71], s[2:3], v71, s0, v[70:71]
	ds_read_b32 v39, v47
	ds_read_b32 v76, v47 offset:1024
	ds_read_b32 v77, v47 offset:2048
	ds_read_b32 v78, v47 offset:3072
	ds_read_b32 v79, v47 offset:4096
	ds_read_b32 v80, v47 offset:5120
	ds_read_b32 v81, v47 offset:6144
	ds_read_b32 v82, v47 offset:7168
	v_mov_b32_e32 v69, v70
	v_lshl_add_u64 v[74:75], v[68:69], 1, v[72:73]
	s_waitcnt lgkmcnt(7)
	v_and_b32_sdwa v68, v39, v66 dst_sel:DWORD dst_unused:UNUSED_PAD src0_sel:WORD_1 src1_sel:DWORD
	v_add3_u32 v39, v39, v68, s31
	s_waitcnt lgkmcnt(4)
	v_and_b32_sdwa v68, v78, v66 dst_sel:DWORD dst_unused:UNUSED_PAD src0_sel:WORD_1 src1_sel:DWORD
	v_and_b32_sdwa v69, v76, v66 dst_sel:DWORD dst_unused:UNUSED_PAD src0_sel:WORD_1 src1_sel:DWORD
	v_and_b32_sdwa v67, v77, v66 dst_sel:DWORD dst_unused:UNUSED_PAD src0_sel:WORD_1 src1_sel:DWORD
	v_add3_u32 v68, v78, v68, s31
	v_add3_u32 v69, v76, v69, s31
	v_add3_u32 v67, v77, v67, s31
	v_and_b32_e32 v68, 0xffff0000, v68
	v_and_b32_e32 v70, 0xffff0000, v69
	v_or_b32_sdwa v69, v68, v67 dst_sel:DWORD dst_unused:UNUSED_PAD src0_sel:DWORD src1_sel:WORD_1
	v_or_b32_sdwa v68, v70, v39 dst_sel:DWORD dst_unused:UNUSED_PAD src0_sel:DWORD src1_sel:WORD_1
	s_waitcnt lgkmcnt(0)
	v_and_b32_sdwa v70, v82, v66 dst_sel:DWORD dst_unused:UNUSED_PAD src0_sel:WORD_1 src1_sel:DWORD
	v_and_b32_sdwa v71, v80, v66 dst_sel:DWORD dst_unused:UNUSED_PAD src0_sel:WORD_1 src1_sel:DWORD
	v_and_b32_sdwa v39, v81, v66 dst_sel:DWORD dst_unused:UNUSED_PAD src0_sel:WORD_1 src1_sel:DWORD
	v_and_b32_sdwa v67, v79, v66 dst_sel:DWORD dst_unused:UNUSED_PAD src0_sel:WORD_1 src1_sel:DWORD
	v_add3_u32 v70, v82, v70, s31
	v_add3_u32 v71, v80, v71, s31
	v_add3_u32 v67, v79, v67, s31
	v_add3_u32 v39, v81, v39, s31
	v_and_b32_e32 v70, 0xffff0000, v70
	v_and_b32_e32 v76, 0xffff0000, v71
	v_or_b32_sdwa v71, v70, v39 dst_sel:DWORD dst_unused:UNUSED_PAD src0_sel:DWORD src1_sel:WORD_1
	v_or_b32_sdwa v70, v76, v67 dst_sel:DWORD dst_unused:UNUSED_PAD src0_sel:DWORD src1_sel:WORD_1
	global_store_dwordx4 v[74:75], v[68:71], off
	ds_read_b32 v39, v50
	ds_read_b32 v67, v50 offset:1024
	ds_read_b32 v76, v50 offset:2048
	ds_read_b32 v77, v50 offset:3072
	ds_read_b32 v78, v50 offset:4096
	ds_read_b32 v79, v50 offset:5120
	ds_read_b32 v80, v50 offset:6144
	ds_read_b32 v81, v50 offset:7168
	v_add_u32_e32 v68, s4, v49
	v_lshlrev_b32_e32 v69, 1, v68
	v_and_b32_e32 v69, 0xffffffe0, v69
	v_add3_u32 v69, s1, v51, v69
	v_cndmask_b32_e32 v68, v69, v68, vcc
	v_ashrrev_i32_e32 v71, 31, v68
	v_mad_u64_u32 v[68:69], s[2:3], v68, s0, 0
	v_mov_b32_e32 v70, v69
	v_mad_u64_u32 v[70:71], s[2:3], v71, s0, v[70:71]
	v_mov_b32_e32 v69, v70
	v_lshl_add_u64 v[74:75], v[68:69], 1, v[72:73]
	s_waitcnt lgkmcnt(7)
	v_and_b32_sdwa v69, v39, v66 dst_sel:DWORD dst_unused:UNUSED_PAD src0_sel:WORD_1 src1_sel:DWORD
	v_add3_u32 v39, v39, v69, s31
	s_waitcnt lgkmcnt(4)
	v_and_b32_sdwa v69, v77, v66 dst_sel:DWORD dst_unused:UNUSED_PAD src0_sel:WORD_1 src1_sel:DWORD
	v_and_b32_sdwa v70, v67, v66 dst_sel:DWORD dst_unused:UNUSED_PAD src0_sel:WORD_1 src1_sel:DWORD
	v_and_b32_sdwa v68, v76, v66 dst_sel:DWORD dst_unused:UNUSED_PAD src0_sel:WORD_1 src1_sel:DWORD
	v_add3_u32 v69, v77, v69, s31
	v_add3_u32 v67, v67, v70, s31
	v_add3_u32 v68, v76, v68, s31
	v_and_b32_e32 v69, 0xffff0000, v69
	v_and_b32_e32 v67, 0xffff0000, v67
	s_waitcnt lgkmcnt(0)
	v_and_b32_sdwa v70, v81, v66 dst_sel:DWORD dst_unused:UNUSED_PAD src0_sel:WORD_1 src1_sel:DWORD
	v_and_b32_sdwa v71, v79, v66 dst_sel:DWORD dst_unused:UNUSED_PAD src0_sel:WORD_1 src1_sel:DWORD
	v_or_b32_sdwa v69, v69, v68 dst_sel:DWORD dst_unused:UNUSED_PAD src0_sel:DWORD src1_sel:WORD_1
	v_or_b32_sdwa v68, v67, v39 dst_sel:DWORD dst_unused:UNUSED_PAD src0_sel:DWORD src1_sel:WORD_1
	v_and_b32_sdwa v39, v80, v66 dst_sel:DWORD dst_unused:UNUSED_PAD src0_sel:WORD_1 src1_sel:DWORD
	v_and_b32_sdwa v67, v78, v66 dst_sel:DWORD dst_unused:UNUSED_PAD src0_sel:WORD_1 src1_sel:DWORD
	v_add3_u32 v70, v81, v70, s31
	v_add3_u32 v71, v79, v71, s31
	v_add3_u32 v67, v78, v67, s31
	v_add3_u32 v39, v80, v39, s31
	v_and_b32_e32 v70, 0xffff0000, v70
	v_and_b32_e32 v76, 0xffff0000, v71
	v_or_b32_sdwa v71, v70, v39 dst_sel:DWORD dst_unused:UNUSED_PAD src0_sel:DWORD src1_sel:WORD_1
	v_or_b32_sdwa v70, v76, v67 dst_sel:DWORD dst_unused:UNUSED_PAD src0_sel:DWORD src1_sel:WORD_1
	global_store_dwordx4 v[74:75], v[68:71], off
	ds_read_b32 v39, v53
	ds_read_b32 v67, v53 offset:1024
	ds_read_b32 v76, v53 offset:2048
	ds_read_b32 v77, v53 offset:3072
	ds_read_b32 v78, v53 offset:4096
	ds_read_b32 v79, v53 offset:5120
	ds_read_b32 v80, v53 offset:6144
	ds_read_b32 v81, v53 offset:7168
	v_add_u32_e32 v68, s4, v52
	v_lshlrev_b32_e32 v69, 1, v68
	v_and_b32_e32 v69, 0xffffffe0, v69
	v_add3_u32 v69, s1, v54, v69
	v_cndmask_b32_e32 v68, v69, v68, vcc
	v_ashrrev_i32_e32 v71, 31, v68
	v_mad_u64_u32 v[68:69], s[2:3], v68, s0, 0
	v_mov_b32_e32 v70, v69
	v_mad_u64_u32 v[70:71], s[2:3], v71, s0, v[70:71]
	v_mov_b32_e32 v69, v70
	v_lshl_add_u64 v[74:75], v[68:69], 1, v[72:73]
	s_waitcnt lgkmcnt(7)
	v_and_b32_sdwa v69, v39, v66 dst_sel:DWORD dst_unused:UNUSED_PAD src0_sel:WORD_1 src1_sel:DWORD
	v_add3_u32 v39, v39, v69, s31
	s_waitcnt lgkmcnt(4)
	v_and_b32_sdwa v69, v77, v66 dst_sel:DWORD dst_unused:UNUSED_PAD src0_sel:WORD_1 src1_sel:DWORD
	v_and_b32_sdwa v70, v67, v66 dst_sel:DWORD dst_unused:UNUSED_PAD src0_sel:WORD_1 src1_sel:DWORD
	v_and_b32_sdwa v68, v76, v66 dst_sel:DWORD dst_unused:UNUSED_PAD src0_sel:WORD_1 src1_sel:DWORD
	v_add3_u32 v69, v77, v69, s31
	v_add3_u32 v67, v67, v70, s31
	v_add3_u32 v68, v76, v68, s31
	v_and_b32_e32 v69, 0xffff0000, v69
	v_and_b32_e32 v67, 0xffff0000, v67
	s_waitcnt lgkmcnt(0)
	v_and_b32_sdwa v70, v81, v66 dst_sel:DWORD dst_unused:UNUSED_PAD src0_sel:WORD_1 src1_sel:DWORD
	v_and_b32_sdwa v71, v79, v66 dst_sel:DWORD dst_unused:UNUSED_PAD src0_sel:WORD_1 src1_sel:DWORD
	v_or_b32_sdwa v69, v69, v68 dst_sel:DWORD dst_unused:UNUSED_PAD src0_sel:DWORD src1_sel:WORD_1
	v_or_b32_sdwa v68, v67, v39 dst_sel:DWORD dst_unused:UNUSED_PAD src0_sel:DWORD src1_sel:WORD_1
	v_and_b32_sdwa v39, v80, v66 dst_sel:DWORD dst_unused:UNUSED_PAD src0_sel:WORD_1 src1_sel:DWORD
	v_and_b32_sdwa v67, v78, v66 dst_sel:DWORD dst_unused:UNUSED_PAD src0_sel:WORD_1 src1_sel:DWORD
	v_add3_u32 v70, v81, v70, s31
	v_add3_u32 v71, v79, v71, s31
	v_add3_u32 v67, v78, v67, s31
	v_add3_u32 v39, v80, v39, s31
	v_and_b32_e32 v70, 0xffff0000, v70
	v_and_b32_e32 v76, 0xffff0000, v71
	v_or_b32_sdwa v71, v70, v39 dst_sel:DWORD dst_unused:UNUSED_PAD src0_sel:DWORD src1_sel:WORD_1
	v_or_b32_sdwa v70, v76, v67 dst_sel:DWORD dst_unused:UNUSED_PAD src0_sel:DWORD src1_sel:WORD_1
	global_store_dwordx4 v[74:75], v[68:71], off
	ds_read_b32 v39, v56
	ds_read_b32 v67, v56 offset:1024
	ds_read_b32 v74, v56 offset:2048
	ds_read_b32 v75, v56 offset:3072
	ds_read_b32 v76, v56 offset:4096
	ds_read_b32 v77, v56 offset:5120
	ds_read_b32 v78, v56 offset:6144
	ds_read_b32 v79, v56 offset:7168
	v_add_u32_e32 v68, s4, v55
	v_lshlrev_b32_e32 v69, 1, v68
	v_and_b32_e32 v69, 0xffffffe0, v69
	v_add3_u32 v69, s1, v57, v69
	v_cndmask_b32_e32 v68, v69, v68, vcc
	v_ashrrev_i32_e32 v71, 31, v68
	v_mad_u64_u32 v[68:69], s[2:3], v68, s0, 0
	v_mov_b32_e32 v70, v69
	v_mad_u64_u32 v[70:71], s[0:1], v71, s0, v[70:71]
	v_mov_b32_e32 v69, v70
	v_lshl_add_u64 v[72:73], v[68:69], 1, v[72:73]
	s_waitcnt lgkmcnt(7)
	v_and_b32_sdwa v69, v39, v66 dst_sel:DWORD dst_unused:UNUSED_PAD src0_sel:WORD_1 src1_sel:DWORD
	v_add3_u32 v39, v39, v69, s31
	s_waitcnt lgkmcnt(4)
	v_and_b32_sdwa v69, v75, v66 dst_sel:DWORD dst_unused:UNUSED_PAD src0_sel:WORD_1 src1_sel:DWORD
	v_and_b32_sdwa v70, v67, v66 dst_sel:DWORD dst_unused:UNUSED_PAD src0_sel:WORD_1 src1_sel:DWORD
	v_and_b32_sdwa v68, v74, v66 dst_sel:DWORD dst_unused:UNUSED_PAD src0_sel:WORD_1 src1_sel:DWORD
	v_add3_u32 v69, v75, v69, s31
	v_add3_u32 v67, v67, v70, s31
	v_add3_u32 v68, v74, v68, s31
	v_and_b32_e32 v69, 0xffff0000, v69
	v_and_b32_e32 v67, 0xffff0000, v67
	s_waitcnt lgkmcnt(0)
	v_and_b32_sdwa v70, v79, v66 dst_sel:DWORD dst_unused:UNUSED_PAD src0_sel:WORD_1 src1_sel:DWORD
	v_and_b32_sdwa v71, v77, v66 dst_sel:DWORD dst_unused:UNUSED_PAD src0_sel:WORD_1 src1_sel:DWORD
	v_or_b32_sdwa v69, v69, v68 dst_sel:DWORD dst_unused:UNUSED_PAD src0_sel:DWORD src1_sel:WORD_1
	v_or_b32_sdwa v68, v67, v39 dst_sel:DWORD dst_unused:UNUSED_PAD src0_sel:DWORD src1_sel:WORD_1
	v_and_b32_sdwa v39, v78, v66 dst_sel:DWORD dst_unused:UNUSED_PAD src0_sel:WORD_1 src1_sel:DWORD
	v_and_b32_sdwa v67, v76, v66 dst_sel:DWORD dst_unused:UNUSED_PAD src0_sel:WORD_1 src1_sel:DWORD
	v_add3_u32 v70, v79, v70, s31
	v_add3_u32 v71, v77, v71, s31
	v_add3_u32 v67, v76, v67, s31
	v_add3_u32 v39, v78, v39, s31
	v_and_b32_e32 v70, 0xffff0000, v70
	v_and_b32_e32 v74, 0xffff0000, v71
	v_or_b32_sdwa v71, v70, v39 dst_sel:DWORD dst_unused:UNUSED_PAD src0_sel:DWORD src1_sel:WORD_1
	v_or_b32_sdwa v70, v74, v67 dst_sel:DWORD dst_unused:UNUSED_PAD src0_sel:DWORD src1_sel:WORD_1
	s_add_i32 s29, s29, 1
	s_and_b64 vcc, exec, s[16:17]
	s_mov_b32 s34, s33
	s_mov_b32 s1, s35
	s_mov_b32 s15, s24
	s_mov_b32 s4, s20
	s_mov_b32 s14, s6
	s_mov_b32 s0, s25
	s_mov_b64 s[2:3], s[18:19]
	global_store_dwordx4 v[72:73], v[68:71], off
	s_barrier
	s_cbranch_vccnz .LBB0_1964
.LBB0_1946:
	s_add_i32 s33, s34, 1
	s_cmp_lt_u32 s30, 2
	s_cselect_b64 s[16:17], -1, 0
	s_and_b64 vcc, exec, s[16:17]
	s_mov_b32 s35, s1
	s_mov_b32 s20, s4
	s_mov_b32 s6, s14
	s_waitcnt vmcnt(0)
	ds_write_b128 v58, v[2:5]
	ds_write_b128 v59, v[6:9]
	ds_write_b128 v60, v[10:13]
	ds_write_b128 v61, v[14:17]
	ds_write_b128 v62, v[18:21]
	ds_write_b128 v63, v[22:25]
	ds_write_b128 v64, v[26:29]
	ds_write_b128 v65, v[30:33]
	s_waitcnt lgkmcnt(0)
	s_barrier
	s_cbranch_vccnz .LBB0_1945
	s_add_i32 s6, s29, 0x93f
	s_cmpk_lt_i32 s6, 0x6bf
	s_cbranch_scc1 .LBB0_1943
	s_add_i32 s6, s29, 0x940
	s_cmpk_gt_u32 s6, 0x83f
	s_mov_b64 s[20:21], -1
	s_cbranch_scc0 .LBB0_1961
	s_cmpk_gt_u32 s6, 0x93f
	s_cbranch_scc0 .LBB0_1958
	s_mul_hi_u32 s6, s29, 0xaaaaaaab
	s_lshr_b32 s6, s6, 8
	s_mul_i32 s18, s6, 0xfffffe80
	s_add_i32 s34, s34, s18
	s_addk_i32 s34, 0xf6c1
	s_add_i32 s38, s29, s18
	s_cmpk_gt_i32 s38, 0x7f
	s_cbranch_scc0 .LBB0_1955
	s_lshl_b64 s[20:21], s[6:7], 23
	s_cmpk_gt_u32 s38, 0xff
	s_mov_b64 s[24:25], -1
	s_cbranch_scc0 .LBB0_1953
	s_add_i32 s37, s34, 0xffffff00
	s_add_u32 s22, s88, s20
	s_addc_u32 s23, s89, s21
	s_lshl_b64 s[18:19], s[6:7], 22
	s_add_u32 s18, s5, s18
	s_addc_u32 s19, s26, s19
	s_mov_b64 s[24:25], 0

.LBB0_1991:
	s_waitcnt vmcnt(11)
	v_add_u32_e32 v2, 0x800, v34
	s_lshr_b32 s0, s8, 8
	v_ashrrev_i32_e32 v42, 6, v2
	v_cvt_f32_u32_e32 v2, s0
	s_sub_i32 s9, 0, s0
	s_abs_i32 s5, s10
	s_ashr_i32 s4, s10, 31
	v_rcp_iflag_f32_e32 v2, v2
	v_add_u32_e32 v3, 0xa00, v34
	v_ashrrev_i32_e32 v43, 6, v3
	v_add_u32_e32 v3, 0xc00, v34
	v_mul_f32_e32 v2, 0x4f7ffffe, v2
	v_cvt_u32_f32_e32 v2, v2
	v_lshlrev_b32_e32 v1, 2, v34
	v_ashrrev_i32_e32 v44, 6, v3
	v_add_u32_e32 v3, 0xe00, v34
	v_readfirstlane_b32 s11, v2
	s_mul_i32 s9, s9, s11
	s_mul_hi_u32 s9, s11, s9
	s_add_i32 s11, s11, s9
	s_mul_hi_u32 s9, s5, s11
	s_mul_i32 s11, s9, s0
	s_sub_i32 s5, s5, s11
	s_add_i32 s11, s9, 1
	s_sub_i32 s12, s5, s0
	s_cmp_ge_u32 s5, s0
	s_cselect_b32 s9, s11, s9
	s_cselect_b32 s5, s12, s5
	s_add_i32 s11, s9, 1
	s_cmp_ge_u32 s5, s0
	s_cselect_b32 s5, s11, s9
	s_xor_b32 s5, s5, s4
	s_sub_i32 s9, s5, s4
	s_mul_i32 s0, s9, s0
	s_sub_i32 s0, s10, s0
	s_lshl_b32 s4, s0, 8
	s_ashr_i32 s5, s4, 31
	s_lshl_b64 s[10:11], s[4:5], 2
	s_add_u32 s6, s6, s10
	v_and_b32_e32 v38, 0xfc, v1
	v_ashrrev_i32_e32 v45, 6, v3
	s_addc_u32 s7, s7, s11
	s_lshl_b32 s14, s9, 6
	v_mov_b32_e32 v37, 0
	v_lshlrev_b32_e32 v36, 2, v38
	v_add_u32_e32 v4, s14, v45
	v_lshl_add_u64 v[2:3], s[6:7], 0, v[36:37]
	s_waitcnt vmcnt(10)
	v_ashrrev_i32_e32 v7, 31, v4
	v_mad_u64_u32 v[4:5], s[6:7], v4, s8, 0
	v_mov_b32_e32 v6, v5
	v_mad_u64_u32 v[6:7], s[6:7], v7, s8, v[6:7]
	v_mov_b32_e32 v5, v6
	v_add_u32_e32 v6, s14, v44
	v_ashrrev_i32_e32 v9, 31, v6
	v_mad_u64_u32 v[6:7], s[6:7], v6, s8, 0
	v_mov_b32_e32 v8, v7
	v_mad_u64_u32 v[8:9], s[6:7], v9, s8, v[8:9]
	v_lshl_add_u64 v[4:5], v[4:5], 2, v[2:3]
	v_mov_b32_e32 v7, v8
	v_lshl_add_u64 v[6:7], v[6:7], 2, v[2:3]
	global_load_dwordx4 v[30:33], v[4:5], off
	global_load_dwordx4 v[26:29], v[6:7], off
	v_add_u32_e32 v4, s14, v43
	v_ashrrev_i32_e32 v7, 31, v4
	v_mad_u64_u32 v[4:5], s[6:7], v4, s8, 0
	v_mov_b32_e32 v6, v5
	v_mad_u64_u32 v[6:7], s[6:7], v7, s8, v[6:7]
	v_mov_b32_e32 v5, v6
	v_add_u32_e32 v6, s14, v42
	v_ashrrev_i32_e32 v9, 31, v6
	v_mad_u64_u32 v[6:7], s[6:7], v6, s8, 0
	v_mov_b32_e32 v8, v7
	v_add_u32_e32 v55, 0x600, v34
	v_mad_u64_u32 v[8:9], s[6:7], v9, s8, v[8:9]
	v_ashrrev_i32_e32 v41, 6, v55
	v_lshl_add_u64 v[4:5], v[4:5], 2, v[2:3]
	v_mov_b32_e32 v7, v8
	v_lshl_add_u64 v[6:7], v[6:7], 2, v[2:3]
	global_load_dwordx4 v[22:25], v[4:5], off
	global_load_dwordx4 v[18:21], v[6:7], off
	v_add_u32_e32 v4, s14, v41
	v_ashrrev_i32_e32 v7, 31, v4
	v_mad_u64_u32 v[4:5], s[6:7], v4, s8, 0
	v_add_u32_e32 v52, 0x400, v34
	v_mov_b32_e32 v6, v5
	v_ashrrev_i32_e32 v40, 6, v52
	v_mad_u64_u32 v[6:7], s[6:7], v7, s8, v[6:7]
	v_mov_b32_e32 v5, v6
	v_add_u32_e32 v6, s14, v40
	v_ashrrev_i32_e32 v9, 31, v6
	v_mad_u64_u32 v[6:7], s[6:7], v6, s8, 0
	v_mov_b32_e32 v8, v7
	v_add_u32_e32 v35, 0x200, v34
	v_mad_u64_u32 v[8:9], s[6:7], v9, s8, v[8:9]
	v_ashrrev_i32_e32 v39, 6, v35
	v_lshl_add_u64 v[4:5], v[4:5], 2, v[2:3]
	v_mov_b32_e32 v7, v8
	v_lshl_add_u64 v[6:7], v[6:7], 2, v[2:3]
	global_load_dwordx4 v[14:17], v[4:5], off
	global_load_dwordx4 v[10:13], v[6:7], off
	v_add_u32_e32 v4, s14, v39
	v_ashrrev_i32_e32 v7, 31, v4
	v_mad_u64_u32 v[4:5], s[6:7], v4, s8, 0
	v_mov_b32_e32 v6, v5
	v_ashrrev_i32_e32 v1, 6, v34
	v_mad_u64_u32 v[6:7], s[6:7], v7, s8, v[6:7]
	v_mov_b32_e32 v5, v6
	v_add_u32_e32 v6, s14, v1
	v_ashrrev_i32_e32 v9, 31, v6
	v_mad_u64_u32 v[6:7], s[6:7], v6, s8, 0
	v_mov_b32_e32 v8, v7
	v_mad_u64_u32 v[8:9], s[6:7], v9, s8, v[8:9]
	v_mov_b32_e32 v7, v8
	v_lshl_add_u64 v[4:5], v[4:5], 2, v[2:3]
	v_lshl_add_u64 v[2:3], v[6:7], 2, v[2:3]
	global_load_dwordx4 v[6:9], v[4:5], off
	s_nop 0
	global_load_dwordx4 v[2:5], v[2:3], off
	v_lshlrev_b32_e32 v46, 3, v34
	v_and_b32_e32 v66, 56, v46
	s_movk_i32 s0, 0x400
	v_readlane_b32 s12, v251, 60
	v_mad_u32_u24 v56, v66, s0, 0
	v_mul_lo_u32 v58, v1, s0
	v_mul_lo_u32 v59, v39, s0
	v_mul_lo_u32 v60, v40, s0
	v_mul_lo_u32 v61, v41, s0
	v_mul_lo_u32 v62, v42, s0
	v_mul_lo_u32 v63, v43, s0
	v_mul_lo_u32 v64, v44, s0
	v_mul_lo_u32 v65, v45, s0
	v_readlane_b32 s13, v251, 61
	s_add_u32 s0, s12, 0x1e940000
	s_addc_u32 s5, s13, 0
	s_add_u32 s8, s12, 0x16940000
	s_addc_u32 s9, s13, 0
	s_add_u32 s10, s12, 0x16140000
	s_addc_u32 s11, s13, 0
	s_add_u32 s27, s12, 0x15540000
	s_addc_u32 s28, s13, 0
	v_add_u32_e32 v36, 0, v36
	v_ashrrev_i32_e32 v46, 3, v34
	v_ashrrev_i32_e32 v49, 3, v35
	v_ashrrev_i32_e32 v52, 3, v52
	v_ashrrev_i32_e32 v55, 3, v55
	s_add_u32 s12, s12, 0x11f40000
	s_mov_b32 s7, 0
	v_xor_b32_e32 v48, v46, v66
	v_lshl_add_u32 v47, v48, 2, v56
	v_and_b32_e32 v48, 15, v46
	v_xor_b32_e32 v51, v49, v66
	v_lshl_add_u32 v50, v51, 2, v56
	v_and_b32_e32 v51, 15, v49
	v_xor_b32_e32 v54, v52, v66
	v_lshl_add_u32 v53, v54, 2, v56
	v_and_b32_e32 v54, 15, v52
	v_xor_b32_e32 v57, v55, v66
	v_lshl_add_u32 v56, v57, 2, v56
	v_and_b32_e32 v57, 15, v55
	s_addc_u32 s13, s13, 0
	s_add_i32 s29, s16, 0xfffffce1
	s_mov_b32 s30, 25
	v_add_u32_e32 v58, v36, v58
	v_add_u32_e32 v59, v36, v59
	v_xor_b32_e32 v59, 32, v59
	v_add_u32_e32 v60, v36, v60
	v_xor_b32_e32 v60, 64, v60
	v_add_u32_e32 v61, v36, v61
	v_xor_b32_e32 v61, 96, v61
	v_add_u32_e32 v62, v36, v62
	v_xor_b32_e32 v62, 128, v62
	v_add_u32_e32 v63, v36, v63
	v_xor_b32_e32 v63, 160, v63
	v_add_u32_e32 v64, v36, v64
	v_xor_b32_e32 v64, 192, v64
	v_add_u32_e32 v65, v36, v65
	v_xor_b32_e32 v65, 224, v65
	v_lshlrev_b32_e32 v36, 2, v38
	v_lshlrev_b32_e32 v34, 1, v66
	s_movk_i32 s31, 0x7fff
	v_mov_b32_e32 v38, 1
	s_mov_b32 s24, s15
	s_mov_b32 s25, s26
	s_mov_b64 s[18:19], s[2:3]
	s_branch .LBB0_1995

.LBB0_1994:
	s_add_i32 s30, s30, -1
	s_cmp_eq_u32 s15, 0
	v_add_u32_e32 v66, s4, v46
	v_lshlrev_b32_e32 v35, 1, v66
	s_cselect_b64 vcc, -1, 0
	s_ashr_i32 s15, s14, 31
	v_and_b32_e32 v35, 0xffffffe0, v35
	s_lshl_b64 s[14:15], s[14:15], 1
	v_add3_u32 v67, s1, v48, v35
	s_add_u32 s2, s2, s14
	s_addc_u32 s3, s3, s15
	v_mov_b32_e32 v35, v37
	v_cndmask_b32_e32 v66, v67, v66, vcc
	v_lshl_add_u64 v[70:71], s[2:3], 0, v[34:35]
	v_ashrrev_i32_e32 v69, 31, v66
	v_mad_u64_u32 v[66:67], s[2:3], v66, s26, 0
	v_mov_b32_e32 v68, v67
	ds_read_b32 v35, v47
	ds_read_b32 v74, v47 offset:1024
	ds_read_b32 v75, v47 offset:2048
	ds_read_b32 v76, v47 offset:3072
	ds_read_b32 v77, v47 offset:4096
	ds_read_b32 v78, v47 offset:5120
	ds_read_b32 v79, v47 offset:6144
	ds_read_b32 v80, v47 offset:7168
	v_mad_u64_u32 v[68:69], s[2:3], v69, s26, v[68:69]
	v_mov_b32_e32 v67, v68
	v_lshl_add_u64 v[72:73], v[66:67], 1, v[70:71]
	s_waitcnt lgkmcnt(7)
	v_and_b32_sdwa v67, v35, v38 dst_sel:DWORD dst_unused:UNUSED_PAD src0_sel:WORD_1 src1_sel:DWORD
	v_add3_u32 v35, v35, v67, s31
	s_waitcnt lgkmcnt(4)
	v_and_b32_sdwa v67, v76, v38 dst_sel:DWORD dst_unused:UNUSED_PAD src0_sel:WORD_1 src1_sel:DWORD
	v_and_b32_sdwa v68, v74, v38 dst_sel:DWORD dst_unused:UNUSED_PAD src0_sel:WORD_1 src1_sel:DWORD
	v_and_b32_sdwa v66, v75, v38 dst_sel:DWORD dst_unused:UNUSED_PAD src0_sel:WORD_1 src1_sel:DWORD
	v_add3_u32 v67, v76, v67, s31
	v_add3_u32 v68, v74, v68, s31
	v_add3_u32 v66, v75, v66, s31
	v_and_b32_e32 v67, 0xffff0000, v67
	v_and_b32_e32 v68, 0xffff0000, v68
	s_waitcnt lgkmcnt(0)
	v_and_b32_sdwa v69, v80, v38 dst_sel:DWORD dst_unused:UNUSED_PAD src0_sel:WORD_1 src1_sel:DWORD
	v_and_b32_sdwa v74, v78, v38 dst_sel:DWORD dst_unused:UNUSED_PAD src0_sel:WORD_1 src1_sel:DWORD
	v_or_b32_sdwa v67, v67, v66 dst_sel:DWORD dst_unused:UNUSED_PAD src0_sel:DWORD src1_sel:WORD_1
	v_or_b32_sdwa v66, v68, v35 dst_sel:DWORD dst_unused:UNUSED_PAD src0_sel:DWORD src1_sel:WORD_1
	v_and_b32_sdwa v35, v79, v38 dst_sel:DWORD dst_unused:UNUSED_PAD src0_sel:WORD_1 src1_sel:DWORD
	v_and_b32_sdwa v68, v77, v38 dst_sel:DWORD dst_unused:UNUSED_PAD src0_sel:WORD_1 src1_sel:DWORD
	v_add3_u32 v69, v80, v69, s31
	v_add3_u32 v74, v78, v74, s31
	v_add3_u32 v68, v77, v68, s31
	v_add3_u32 v35, v79, v35, s31
	v_and_b32_e32 v69, 0xffff0000, v69
	v_and_b32_e32 v74, 0xffff0000, v74
	v_or_b32_sdwa v69, v69, v35 dst_sel:DWORD dst_unused:UNUSED_PAD src0_sel:DWORD src1_sel:WORD_1
	v_or_b32_sdwa v68, v74, v68 dst_sel:DWORD dst_unused:UNUSED_PAD src0_sel:DWORD src1_sel:WORD_1
	global_store_dwordx4 v[72:73], v[66:69], off
	ds_read_b32 v35, v50
	ds_read_b32 v74, v50 offset:1024
	ds_read_b32 v75, v50 offset:2048
	ds_read_b32 v76, v50 offset:3072
	ds_read_b32 v77, v50 offset:4096
	ds_read_b32 v78, v50 offset:5120
	ds_read_b32 v79, v50 offset:6144
	ds_read_b32 v80, v50 offset:7168
	v_add_u32_e32 v66, s4, v49
	v_lshlrev_b32_e32 v67, 1, v66
	v_and_b32_e32 v67, 0xffffffe0, v67
	v_add3_u32 v67, s1, v51, v67
	v_cndmask_b32_e32 v66, v67, v66, vcc
	v_ashrrev_i32_e32 v69, 31, v66
	v_mad_u64_u32 v[66:67], s[2:3], v66, s26, 0
	v_mov_b32_e32 v68, v67
	v_mad_u64_u32 v[68:69], s[2:3], v69, s26, v[68:69]
	v_mov_b32_e32 v67, v68
	v_lshl_add_u64 v[72:73], v[66:67], 1, v[70:71]
	s_waitcnt lgkmcnt(7)
	v_and_b32_sdwa v67, v35, v38 dst_sel:DWORD dst_unused:UNUSED_PAD src0_sel:WORD_1 src1_sel:DWORD
	v_add3_u32 v35, v35, v67, s31
	s_waitcnt lgkmcnt(4)
	v_and_b32_sdwa v67, v76, v38 dst_sel:DWORD dst_unused:UNUSED_PAD src0_sel:WORD_1 src1_sel:DWORD
	v_and_b32_sdwa v68, v74, v38 dst_sel:DWORD dst_unused:UNUSED_PAD src0_sel:WORD_1 src1_sel:DWORD
	v_and_b32_sdwa v66, v75, v38 dst_sel:DWORD dst_unused:UNUSED_PAD src0_sel:WORD_1 src1_sel:DWORD
	v_add3_u32 v67, v76, v67, s31
	v_add3_u32 v68, v74, v68, s31
	v_add3_u32 v66, v75, v66, s31
	v_and_b32_e32 v67, 0xffff0000, v67
	v_and_b32_e32 v68, 0xffff0000, v68
	s_waitcnt lgkmcnt(0)
	v_and_b32_sdwa v69, v80, v38 dst_sel:DWORD dst_unused:UNUSED_PAD src0_sel:WORD_1 src1_sel:DWORD
	v_and_b32_sdwa v74, v78, v38 dst_sel:DWORD dst_unused:UNUSED_PAD src0_sel:WORD_1 src1_sel:DWORD
	v_or_b32_sdwa v67, v67, v66 dst_sel:DWORD dst_unused:UNUSED_PAD src0_sel:DWORD src1_sel:WORD_1
	v_or_b32_sdwa v66, v68, v35 dst_sel:DWORD dst_unused:UNUSED_PAD src0_sel:DWORD src1_sel:WORD_1
	v_and_b32_sdwa v35, v79, v38 dst_sel:DWORD dst_unused:UNUSED_PAD src0_sel:WORD_1 src1_sel:DWORD
	v_and_b32_sdwa v68, v77, v38 dst_sel:DWORD dst_unused:UNUSED_PAD src0_sel:WORD_1 src1_sel:DWORD
	v_add3_u32 v69, v80, v69, s31
	v_add3_u32 v74, v78, v74, s31
	v_add3_u32 v68, v77, v68, s31
	v_add3_u32 v35, v79, v35, s31
	v_and_b32_e32 v69, 0xffff0000, v69
	v_and_b32_e32 v74, 0xffff0000, v74
	v_or_b32_sdwa v69, v69, v35 dst_sel:DWORD dst_unused:UNUSED_PAD src0_sel:DWORD src1_sel:WORD_1
	v_or_b32_sdwa v68, v74, v68 dst_sel:DWORD dst_unused:UNUSED_PAD src0_sel:DWORD src1_sel:WORD_1
	global_store_dwordx4 v[72:73], v[66:69], off
	ds_read_b32 v35, v53
	ds_read_b32 v74, v53 offset:1024
	ds_read_b32 v75, v53 offset:2048
	ds_read_b32 v76, v53 offset:3072
	ds_read_b32 v77, v53 offset:4096
	ds_read_b32 v78, v53 offset:5120
	ds_read_b32 v79, v53 offset:6144
	ds_read_b32 v80, v53 offset:7168
	v_add_u32_e32 v66, s4, v52
	v_lshlrev_b32_e32 v67, 1, v66
	v_and_b32_e32 v67, 0xffffffe0, v67
	v_add3_u32 v67, s1, v54, v67
	v_cndmask_b32_e32 v66, v67, v66, vcc
	v_ashrrev_i32_e32 v69, 31, v66
	v_mad_u64_u32 v[66:67], s[2:3], v66, s26, 0
	v_mov_b32_e32 v68, v67
	v_mad_u64_u32 v[68:69], s[2:3], v69, s26, v[68:69]
	v_mov_b32_e32 v67, v68
	v_lshl_add_u64 v[72:73], v[66:67], 1, v[70:71]
	s_waitcnt lgkmcnt(7)
	v_and_b32_sdwa v67, v35, v38 dst_sel:DWORD dst_unused:UNUSED_PAD src0_sel:WORD_1 src1_sel:DWORD
	v_add3_u32 v35, v35, v67, s31
	s_waitcnt lgkmcnt(4)
	v_and_b32_sdwa v67, v76, v38 dst_sel:DWORD dst_unused:UNUSED_PAD src0_sel:WORD_1 src1_sel:DWORD
	v_and_b32_sdwa v68, v74, v38 dst_sel:DWORD dst_unused:UNUSED_PAD src0_sel:WORD_1 src1_sel:DWORD
	v_and_b32_sdwa v66, v75, v38 dst_sel:DWORD dst_unused:UNUSED_PAD src0_sel:WORD_1 src1_sel:DWORD
	v_add3_u32 v67, v76, v67, s31
	v_add3_u32 v68, v74, v68, s31
	v_add3_u32 v66, v75, v66, s31
	v_and_b32_e32 v67, 0xffff0000, v67
	v_and_b32_e32 v68, 0xffff0000, v68
	s_waitcnt lgkmcnt(0)
	v_and_b32_sdwa v69, v80, v38 dst_sel:DWORD dst_unused:UNUSED_PAD src0_sel:WORD_1 src1_sel:DWORD
	v_and_b32_sdwa v74, v78, v38 dst_sel:DWORD dst_unused:UNUSED_PAD src0_sel:WORD_1 src1_sel:DWORD
	v_or_b32_sdwa v67, v67, v66 dst_sel:DWORD dst_unused:UNUSED_PAD src0_sel:DWORD src1_sel:WORD_1
	v_or_b32_sdwa v66, v68, v35 dst_sel:DWORD dst_unused:UNUSED_PAD src0_sel:DWORD src1_sel:WORD_1
	v_and_b32_sdwa v35, v79, v38 dst_sel:DWORD dst_unused:UNUSED_PAD src0_sel:WORD_1 src1_sel:DWORD
	v_and_b32_sdwa v68, v77, v38 dst_sel:DWORD dst_unused:UNUSED_PAD src0_sel:WORD_1 src1_sel:DWORD
	v_add3_u32 v69, v80, v69, s31
	v_add3_u32 v74, v78, v74, s31
	v_add3_u32 v68, v77, v68, s31
	v_add3_u32 v35, v79, v35, s31
	v_and_b32_e32 v69, 0xffff0000, v69
	v_and_b32_e32 v74, 0xffff0000, v74
	v_or_b32_sdwa v69, v69, v35 dst_sel:DWORD dst_unused:UNUSED_PAD src0_sel:DWORD src1_sel:WORD_1
	v_or_b32_sdwa v68, v74, v68 dst_sel:DWORD dst_unused:UNUSED_PAD src0_sel:DWORD src1_sel:WORD_1
	global_store_dwordx4 v[72:73], v[66:69], off
	ds_read_b32 v35, v56
	ds_read_b32 v72, v56 offset:1024
	ds_read_b32 v73, v56 offset:2048
	ds_read_b32 v74, v56 offset:3072
	ds_read_b32 v75, v56 offset:4096
	ds_read_b32 v76, v56 offset:5120
	ds_read_b32 v77, v56 offset:6144
	ds_read_b32 v78, v56 offset:7168
	v_add_u32_e32 v66, s4, v55
	v_lshlrev_b32_e32 v67, 1, v66
	v_and_b32_e32 v67, 0xffffffe0, v67
	v_add3_u32 v67, s1, v57, v67
	v_cndmask_b32_e32 v66, v67, v66, vcc
	v_ashrrev_i32_e32 v69, 31, v66
	v_mad_u64_u32 v[66:67], s[2:3], v66, s26, 0
	v_mov_b32_e32 v68, v67
	v_mad_u64_u32 v[68:69], s[2:3], v69, s26, v[68:69]
	v_mov_b32_e32 v67, v68
	v_lshl_add_u64 v[70:71], v[66:67], 1, v[70:71]
	s_waitcnt lgkmcnt(7)
	v_and_b32_sdwa v67, v35, v38 dst_sel:DWORD dst_unused:UNUSED_PAD src0_sel:WORD_1 src1_sel:DWORD
	v_add3_u32 v35, v35, v67, s31
	s_waitcnt lgkmcnt(4)
	v_and_b32_sdwa v67, v74, v38 dst_sel:DWORD dst_unused:UNUSED_PAD src0_sel:WORD_1 src1_sel:DWORD
	v_and_b32_sdwa v68, v72, v38 dst_sel:DWORD dst_unused:UNUSED_PAD src0_sel:WORD_1 src1_sel:DWORD
	v_and_b32_sdwa v66, v73, v38 dst_sel:DWORD dst_unused:UNUSED_PAD src0_sel:WORD_1 src1_sel:DWORD
	v_add3_u32 v67, v74, v67, s31
	v_add3_u32 v68, v72, v68, s31
	v_add3_u32 v66, v73, v66, s31
	v_and_b32_e32 v67, 0xffff0000, v67
	v_and_b32_e32 v68, 0xffff0000, v68
	s_waitcnt lgkmcnt(0)
	v_and_b32_sdwa v69, v78, v38 dst_sel:DWORD dst_unused:UNUSED_PAD src0_sel:WORD_1 src1_sel:DWORD
	v_and_b32_sdwa v72, v76, v38 dst_sel:DWORD dst_unused:UNUSED_PAD src0_sel:WORD_1 src1_sel:DWORD
	v_or_b32_sdwa v67, v67, v66 dst_sel:DWORD dst_unused:UNUSED_PAD src0_sel:DWORD src1_sel:WORD_1
	v_or_b32_sdwa v66, v68, v35 dst_sel:DWORD dst_unused:UNUSED_PAD src0_sel:DWORD src1_sel:WORD_1
	v_and_b32_sdwa v35, v77, v38 dst_sel:DWORD dst_unused:UNUSED_PAD src0_sel:WORD_1 src1_sel:DWORD
	v_and_b32_sdwa v68, v75, v38 dst_sel:DWORD dst_unused:UNUSED_PAD src0_sel:WORD_1 src1_sel:DWORD
	v_add3_u32 v69, v78, v69, s31
	v_add3_u32 v72, v76, v72, s31
	v_add3_u32 v68, v75, v68, s31
	v_add3_u32 v35, v77, v35, s31
	v_and_b32_e32 v69, 0xffff0000, v69
	v_and_b32_e32 v72, 0xffff0000, v72
	v_or_b32_sdwa v69, v69, v35 dst_sel:DWORD dst_unused:UNUSED_PAD src0_sel:DWORD src1_sel:WORD_1
	v_or_b32_sdwa v68, v72, v68 dst_sel:DWORD dst_unused:UNUSED_PAD src0_sel:DWORD src1_sel:WORD_1
	s_add_i32 s29, s29, 1
	s_and_b64 vcc, exec, s[16:17]
	s_mov_b32 s34, s33
	s_mov_b32 s1, s35
	s_mov_b32 s15, s24
	s_mov_b32 s4, s20
	s_mov_b32 s14, s6
	s_mov_b32 s26, s25
	s_mov_b64 s[2:3], s[18:19]
	global_store_dwordx4 v[70:71], v[66:69], off
	s_barrier
	s_cbranch_vccnz .LBB0_2013
.LBB0_1995:
	s_add_i32 s33, s34, 1
	s_cmp_lt_u32 s30, 2
	s_cselect_b64 s[16:17], -1, 0
	s_and_b64 vcc, exec, s[16:17]
	s_mov_b32 s35, s1
	s_mov_b32 s20, s4
	s_mov_b32 s6, s14
	s_waitcnt vmcnt(0)
	ds_write_b128 v58, v[2:5]
	ds_write_b128 v59, v[6:9]
	ds_write_b128 v60, v[10:13]
	ds_write_b128 v61, v[14:17]
	ds_write_b128 v62, v[18:21]
	ds_write_b128 v63, v[22:25]
	ds_write_b128 v64, v[26:29]
	ds_write_b128 v65, v[30:33]
	s_waitcnt lgkmcnt(0)
	s_barrier
	s_cbranch_vccnz .LBB0_1994
	s_add_i32 s6, s29, 0x93f
	s_cmpk_lt_i32 s6, 0x6bf
	s_cbranch_scc1 .LBB0_1992
	s_add_i32 s6, s29, 0x940
	s_cmpk_gt_u32 s6, 0x83f
	s_mov_b64 s[20:21], -1
	s_cbranch_scc0 .LBB0_2010
	s_cmpk_gt_u32 s6, 0x93f
	s_cbranch_scc0 .LBB0_2007
	s_mul_hi_u32 s6, s29, 0xaaaaaaab
	s_lshr_b32 s6, s6, 8
	s_mul_i32 s18, s6, 0xfffffe80
	s_add_i32 s34, s34, s18
	s_addk_i32 s34, 0xf6c1
	s_add_i32 s38, s29, s18
	s_cmpk_gt_i32 s38, 0x7f
	s_cbranch_scc0 .LBB0_2004
	s_lshl_b64 s[20:21], s[6:7], 23
	s_cmpk_gt_u32 s38, 0xff
	s_mov_b64 s[24:25], -1
	s_cbranch_scc0 .LBB0_2002
	s_add_i32 s37, s34, 0xffffff00
	s_add_u32 s22, s88, s20
	s_addc_u32 s23, s89, s21
	s_lshl_b64 s[18:19], s[6:7], 22
	s_add_u32 s18, s0, s18
	s_addc_u32 s19, s5, s19
	s_mov_b64 s[24:25], 0

.LBB0_2313:
	s_waitcnt vmcnt(11)
	v_add_u32_e32 v2, 0x800, v130
	s_lshr_b32 s0, s12, 8
	v_ashrrev_i32_e32 v41, 6, v2
	v_cvt_f32_u32_e32 v2, s0
	s_sub_i32 s14, 0, s0
	s_abs_i32 s9, s13
	s_ashr_i32 s8, s13, 31
	v_rcp_iflag_f32_e32 v2, v2
	v_add_u32_e32 v3, 0xa00, v130
	v_ashrrev_i32_e32 v42, 6, v3
	v_add_u32_e32 v3, 0xc00, v130
	v_mul_f32_e32 v2, 0x4f7ffffe, v2
	v_cvt_u32_f32_e32 v2, v2
	v_lshlrev_b32_e32 v1, 2, v130
	v_ashrrev_i32_e32 v43, 6, v3
	v_add_u32_e32 v3, 0xe00, v130
	v_readfirstlane_b32 s15, v2
	s_mul_i32 s14, s14, s15
	s_mul_hi_u32 s14, s15, s14
	s_add_i32 s15, s15, s14
	s_mul_hi_u32 s14, s9, s15
	s_mul_i32 s15, s14, s0
	s_sub_i32 s9, s9, s15
	s_add_i32 s15, s14, 1
	s_sub_i32 s16, s9, s0
	s_cmp_ge_u32 s9, s0
	s_cselect_b32 s14, s15, s14
	s_cselect_b32 s9, s16, s9
	s_add_i32 s15, s14, 1
	s_cmp_ge_u32 s9, s0
	s_cselect_b32 s9, s15, s14
	s_xor_b32 s9, s9, s8
	s_sub_i32 s16, s9, s8
	s_mul_i32 s0, s16, s0
	s_sub_i32 s0, s13, s0
	s_lshl_b32 s8, s0, 8
	s_ashr_i32 s9, s8, 31
	s_lshl_b64 s[14:15], s[8:9], 2
	s_add_u32 s10, s10, s14
	v_and_b32_e32 v36, 0xfc, v1
	v_ashrrev_i32_e32 v44, 6, v3
	s_addc_u32 s11, s11, s15
	s_lshl_b32 s20, s16, 6
	v_mov_b32_e32 v35, 0
	v_lshlrev_b32_e32 v34, 2, v36
	v_add_u32_e32 v4, s20, v44
	v_lshl_add_u64 v[2:3], s[10:11], 0, v[34:35]
	s_waitcnt vmcnt(10)
	v_ashrrev_i32_e32 v7, 31, v4
	v_mad_u64_u32 v[4:5], s[10:11], v4, s12, 0
	v_mov_b32_e32 v6, v5
	v_mad_u64_u32 v[6:7], s[10:11], v7, s12, v[6:7]
	v_mov_b32_e32 v5, v6
	v_add_u32_e32 v6, s20, v43
	v_ashrrev_i32_e32 v9, 31, v6
	v_mad_u64_u32 v[6:7], s[10:11], v6, s12, 0
	v_mov_b32_e32 v8, v7
	v_mad_u64_u32 v[8:9], s[10:11], v9, s12, v[8:9]
	v_lshl_add_u64 v[4:5], v[4:5], 2, v[2:3]
	v_mov_b32_e32 v7, v8
	v_lshl_add_u64 v[6:7], v[6:7], 2, v[2:3]
	global_load_dwordx4 v[30:33], v[4:5], off
	global_load_dwordx4 v[26:29], v[6:7], off
	v_add_u32_e32 v4, s20, v42
	v_ashrrev_i32_e32 v7, 31, v4
	v_mad_u64_u32 v[4:5], s[10:11], v4, s12, 0
	v_mov_b32_e32 v6, v5
	v_mad_u64_u32 v[6:7], s[10:11], v7, s12, v[6:7]
	v_mov_b32_e32 v5, v6
	v_add_u32_e32 v6, s20, v41
	v_ashrrev_i32_e32 v9, 31, v6
	v_mad_u64_u32 v[6:7], s[10:11], v6, s12, 0
	v_mov_b32_e32 v8, v7
	v_add_u32_e32 v54, 0x600, v130
	v_mad_u64_u32 v[8:9], s[10:11], v9, s12, v[8:9]
	v_ashrrev_i32_e32 v40, 6, v54
	v_lshl_add_u64 v[4:5], v[4:5], 2, v[2:3]
	v_mov_b32_e32 v7, v8
	v_lshl_add_u64 v[6:7], v[6:7], 2, v[2:3]
	global_load_dwordx4 v[22:25], v[4:5], off
	global_load_dwordx4 v[18:21], v[6:7], off
	v_add_u32_e32 v4, s20, v40
	v_ashrrev_i32_e32 v7, 31, v4
	v_mad_u64_u32 v[4:5], s[10:11], v4, s12, 0
	v_add_u32_e32 v51, 0x400, v130
	v_mov_b32_e32 v6, v5
	v_ashrrev_i32_e32 v39, 6, v51
	v_mad_u64_u32 v[6:7], s[10:11], v7, s12, v[6:7]
	v_mov_b32_e32 v5, v6
	v_add_u32_e32 v6, s20, v39
	v_ashrrev_i32_e32 v9, 31, v6
	v_mad_u64_u32 v[6:7], s[10:11], v6, s12, 0
	v_mov_b32_e32 v8, v7
	v_add_u32_e32 v37, 0x200, v130
	v_mad_u64_u32 v[8:9], s[10:11], v9, s12, v[8:9]
	v_ashrrev_i32_e32 v38, 6, v37
	v_lshl_add_u64 v[4:5], v[4:5], 2, v[2:3]
	v_mov_b32_e32 v7, v8
	v_lshl_add_u64 v[6:7], v[6:7], 2, v[2:3]
	global_load_dwordx4 v[14:17], v[4:5], off
	global_load_dwordx4 v[10:13], v[6:7], off
	v_add_u32_e32 v4, s20, v38
	v_ashrrev_i32_e32 v7, 31, v4
	v_mad_u64_u32 v[4:5], s[10:11], v4, s12, 0
	v_mov_b32_e32 v6, v5
	v_ashrrev_i32_e32 v1, 6, v130
	v_mad_u64_u32 v[6:7], s[10:11], v7, s12, v[6:7]
	v_mov_b32_e32 v5, v6
	v_add_u32_e32 v6, s20, v1
	v_ashrrev_i32_e32 v9, 31, v6
	v_mad_u64_u32 v[6:7], s[10:11], v6, s12, 0
	v_mov_b32_e32 v8, v7
	v_mad_u64_u32 v[8:9], s[10:11], v9, s12, v[8:9]
	v_mov_b32_e32 v7, v8
	v_lshl_add_u64 v[4:5], v[4:5], 2, v[2:3]
	v_lshl_add_u64 v[2:3], v[6:7], 2, v[2:3]
	global_load_dwordx4 v[6:9], v[4:5], off
	s_nop 0
	global_load_dwordx4 v[2:5], v[2:3], off
	v_lshlrev_b32_e32 v45, 3, v130
	v_and_b32_e32 v66, 56, v45
	s_movk_i32 s0, 0x400
	v_mad_u32_u24 v55, v66, s0, 0
	v_mul_lo_u32 v57, v1, s0
	v_mul_lo_u32 v58, v38, s0
	v_mul_lo_u32 v59, v39, s0
	v_mul_lo_u32 v60, v40, s0
	v_mul_lo_u32 v61, v41, s0
	v_mul_lo_u32 v62, v42, s0
	v_mul_lo_u32 v63, v43, s0
	v_mul_lo_u32 v64, v44, s0
	s_add_u32 s0, s6, 0x1e940000
	s_addc_u32 s9, s7, 0
	s_add_u32 s12, s6, 0x16940000
	s_addc_u32 s13, s7, 0
	s_add_u32 s14, s78, 0x1000000
	s_addc_u32 s15, s79, 0
	s_add_u32 s16, s6, 0x16140000
	s_addc_u32 s17, s7, 0
	v_readlane_b32 s56, v250, 7
	s_add_u32 s36, s6, 0x15540000
	v_readlane_b32 s70, v250, 21
	v_readlane_b32 s71, v250, 22
	s_addc_u32 s37, s7, 0
	s_mov_b64 s[18:19], s[70:71]
	s_add_u32 s18, s18, 0x6c00000
	s_addc_u32 s19, s19, 0
	s_add_u32 s6, s6, 0x11f40000
	v_add_u32_e32 v34, 0, v34
	v_ashrrev_i32_e32 v45, 3, v130
	v_ashrrev_i32_e32 v48, 3, v37
	v_ashrrev_i32_e32 v51, 3, v51
	v_ashrrev_i32_e32 v54, 3, v54
	s_addc_u32 s7, s7, 0
	s_add_i32 s10, s33, s40
	s_mov_b32 s11, 0
	v_xor_b32_e32 v47, v45, v66
	v_lshl_add_u32 v46, v47, 2, v55
	v_and_b32_e32 v47, 15, v45
	v_xor_b32_e32 v50, v48, v66
	v_lshl_add_u32 v49, v50, 2, v55
	v_and_b32_e32 v50, 15, v48
	v_xor_b32_e32 v53, v51, v66
	v_lshl_add_u32 v52, v53, 2, v55
	v_and_b32_e32 v53, 15, v51
	v_xor_b32_e32 v56, v54, v66
	v_lshl_add_u32 v55, v56, 2, v55
	v_and_b32_e32 v56, 15, v54
	s_add_i32 s38, s10, 0xfffff5c0
	s_add_i32 s39, s10, 0xfffff6c0
	v_add_u32_e32 v57, v34, v57
	v_add_u32_e32 v58, v34, v58
	v_xor_b32_e32 v58, 32, v58
	v_add_u32_e32 v59, v34, v59
	v_xor_b32_e32 v59, 64, v59
	v_add_u32_e32 v60, v34, v60
	v_xor_b32_e32 v60, 96, v60
	v_add_u32_e32 v61, v34, v61
	v_xor_b32_e32 v61, 128, v61
	v_add_u32_e32 v62, v34, v62
	v_xor_b32_e32 v62, 160, v62
	v_add_u32_e32 v63, v34, v63
	v_xor_b32_e32 v63, 192, v63
	v_add_u32_e32 v64, v34, v64
	v_xor_b32_e32 v64, 224, v64
	v_lshlrev_b32_e32 v34, 2, v36
	v_lshlrev_b32_e32 v36, 1, v66
	s_movk_i32 s41, 0x7fff
	v_mov_b32_e32 v65, 1
	s_mov_b32 s10, s21
	s_mov_b32 s42, s35
	s_mov_b64 s[24:25], s[2:3]
	v_readlane_b32 s57, v250, 8
	v_readlane_b32 s58, v250, 9
	v_readlane_b32 s59, v250, 10
	v_readlane_b32 s60, v250, 11
	v_readlane_b32 s61, v250, 12
	v_readlane_b32 s62, v250, 13
	v_readlane_b32 s63, v250, 14
	v_readlane_b32 s64, v250, 15
	v_readlane_b32 s65, v250, 16
	v_readlane_b32 s66, v250, 17
	v_readlane_b32 s67, v250, 18
	v_readlane_b32 s68, v250, 19
	v_readlane_b32 s69, v250, 20
	s_branch .LBB0_2317

.LBB0_2316:
	s_add_i32 s34, s34, -1
	s_cmp_eq_u32 s21, 0
	v_add_u32_e32 v66, s8, v45
	v_lshlrev_b32_e32 v37, 1, v66
	s_cselect_b64 vcc, -1, 0
	s_ashr_i32 s21, s20, 31
	v_and_b32_e32 v37, 0xffffffe0, v37
	s_lshl_b64 s[20:21], s[20:21], 1
	v_add3_u32 v67, s1, v47, v37
	s_add_u32 s2, s2, s20
	s_addc_u32 s3, s3, s21
	v_mov_b32_e32 v37, v35
	v_cndmask_b32_e32 v66, v67, v66, vcc
	v_lshl_add_u64 v[70:71], s[2:3], 0, v[36:37]
	v_ashrrev_i32_e32 v69, 31, v66
	v_mad_u64_u32 v[66:67], s[2:3], v66, s35, 0
	v_mov_b32_e32 v68, v67
	ds_read_b32 v37, v46
	ds_read_b32 v74, v46 offset:1024
	ds_read_b32 v75, v46 offset:2048
	ds_read_b32 v76, v46 offset:3072
	ds_read_b32 v77, v46 offset:4096
	ds_read_b32 v78, v46 offset:5120
	ds_read_b32 v79, v46 offset:6144
	ds_read_b32 v80, v46 offset:7168
	v_mad_u64_u32 v[68:69], s[2:3], v69, s35, v[68:69]
	v_mov_b32_e32 v67, v68
	v_lshl_add_u64 v[72:73], v[66:67], 1, v[70:71]
	s_waitcnt lgkmcnt(7)
	v_and_b32_sdwa v67, v37, v65 dst_sel:DWORD dst_unused:UNUSED_PAD src0_sel:WORD_1 src1_sel:DWORD
	v_add3_u32 v37, v37, v67, s41
	s_waitcnt lgkmcnt(4)
	v_and_b32_sdwa v67, v76, v65 dst_sel:DWORD dst_unused:UNUSED_PAD src0_sel:WORD_1 src1_sel:DWORD
	v_and_b32_sdwa v68, v74, v65 dst_sel:DWORD dst_unused:UNUSED_PAD src0_sel:WORD_1 src1_sel:DWORD
	v_and_b32_sdwa v66, v75, v65 dst_sel:DWORD dst_unused:UNUSED_PAD src0_sel:WORD_1 src1_sel:DWORD
	v_add3_u32 v67, v76, v67, s41
	v_add3_u32 v68, v74, v68, s41
	v_add3_u32 v66, v75, v66, s41
	v_and_b32_e32 v67, 0xffff0000, v67
	v_and_b32_e32 v68, 0xffff0000, v68
	s_waitcnt lgkmcnt(0)
	v_and_b32_sdwa v69, v80, v65 dst_sel:DWORD dst_unused:UNUSED_PAD src0_sel:WORD_1 src1_sel:DWORD
	v_and_b32_sdwa v74, v78, v65 dst_sel:DWORD dst_unused:UNUSED_PAD src0_sel:WORD_1 src1_sel:DWORD
	v_or_b32_sdwa v67, v67, v66 dst_sel:DWORD dst_unused:UNUSED_PAD src0_sel:DWORD src1_sel:WORD_1
	v_or_b32_sdwa v66, v68, v37 dst_sel:DWORD dst_unused:UNUSED_PAD src0_sel:DWORD src1_sel:WORD_1
	v_and_b32_sdwa v37, v79, v65 dst_sel:DWORD dst_unused:UNUSED_PAD src0_sel:WORD_1 src1_sel:DWORD
	v_and_b32_sdwa v68, v77, v65 dst_sel:DWORD dst_unused:UNUSED_PAD src0_sel:WORD_1 src1_sel:DWORD
	v_add3_u32 v69, v80, v69, s41
	v_add3_u32 v74, v78, v74, s41
	v_add3_u32 v68, v77, v68, s41
	v_add3_u32 v37, v79, v37, s41
	v_and_b32_e32 v69, 0xffff0000, v69
	v_and_b32_e32 v74, 0xffff0000, v74
	v_or_b32_sdwa v69, v69, v37 dst_sel:DWORD dst_unused:UNUSED_PAD src0_sel:DWORD src1_sel:WORD_1
	v_or_b32_sdwa v68, v74, v68 dst_sel:DWORD dst_unused:UNUSED_PAD src0_sel:DWORD src1_sel:WORD_1
	global_store_dwordx4 v[72:73], v[66:69], off
	ds_read_b32 v37, v49
	ds_read_b32 v74, v49 offset:1024
	ds_read_b32 v75, v49 offset:2048
	ds_read_b32 v76, v49 offset:3072
	ds_read_b32 v77, v49 offset:4096
	ds_read_b32 v78, v49 offset:5120
	ds_read_b32 v79, v49 offset:6144
	ds_read_b32 v80, v49 offset:7168
	v_add_u32_e32 v66, s8, v48
	v_lshlrev_b32_e32 v67, 1, v66
	v_and_b32_e32 v67, 0xffffffe0, v67
	v_add3_u32 v67, s1, v50, v67
	v_cndmask_b32_e32 v66, v67, v66, vcc
	v_ashrrev_i32_e32 v69, 31, v66
	v_mad_u64_u32 v[66:67], s[2:3], v66, s35, 0
	v_mov_b32_e32 v68, v67
	v_mad_u64_u32 v[68:69], s[2:3], v69, s35, v[68:69]
	v_mov_b32_e32 v67, v68
	v_lshl_add_u64 v[72:73], v[66:67], 1, v[70:71]
	s_waitcnt lgkmcnt(7)
	v_and_b32_sdwa v67, v37, v65 dst_sel:DWORD dst_unused:UNUSED_PAD src0_sel:WORD_1 src1_sel:DWORD
	v_add3_u32 v37, v37, v67, s41
	s_waitcnt lgkmcnt(4)
	v_and_b32_sdwa v67, v76, v65 dst_sel:DWORD dst_unused:UNUSED_PAD src0_sel:WORD_1 src1_sel:DWORD
	v_and_b32_sdwa v68, v74, v65 dst_sel:DWORD dst_unused:UNUSED_PAD src0_sel:WORD_1 src1_sel:DWORD
	v_and_b32_sdwa v66, v75, v65 dst_sel:DWORD dst_unused:UNUSED_PAD src0_sel:WORD_1 src1_sel:DWORD
	v_add3_u32 v67, v76, v67, s41
	v_add3_u32 v68, v74, v68, s41
	v_add3_u32 v66, v75, v66, s41
	v_and_b32_e32 v67, 0xffff0000, v67
	v_and_b32_e32 v68, 0xffff0000, v68
	s_waitcnt lgkmcnt(0)
	v_and_b32_sdwa v69, v80, v65 dst_sel:DWORD dst_unused:UNUSED_PAD src0_sel:WORD_1 src1_sel:DWORD
	v_and_b32_sdwa v74, v78, v65 dst_sel:DWORD dst_unused:UNUSED_PAD src0_sel:WORD_1 src1_sel:DWORD
	v_or_b32_sdwa v67, v67, v66 dst_sel:DWORD dst_unused:UNUSED_PAD src0_sel:DWORD src1_sel:WORD_1
	v_or_b32_sdwa v66, v68, v37 dst_sel:DWORD dst_unused:UNUSED_PAD src0_sel:DWORD src1_sel:WORD_1
	v_and_b32_sdwa v37, v79, v65 dst_sel:DWORD dst_unused:UNUSED_PAD src0_sel:WORD_1 src1_sel:DWORD
	v_and_b32_sdwa v68, v77, v65 dst_sel:DWORD dst_unused:UNUSED_PAD src0_sel:WORD_1 src1_sel:DWORD
	v_add3_u32 v69, v80, v69, s41
	v_add3_u32 v74, v78, v74, s41
	v_add3_u32 v68, v77, v68, s41
	v_add3_u32 v37, v79, v37, s41
	v_and_b32_e32 v69, 0xffff0000, v69
	v_and_b32_e32 v74, 0xffff0000, v74
	v_or_b32_sdwa v69, v69, v37 dst_sel:DWORD dst_unused:UNUSED_PAD src0_sel:DWORD src1_sel:WORD_1
	v_or_b32_sdwa v68, v74, v68 dst_sel:DWORD dst_unused:UNUSED_PAD src0_sel:DWORD src1_sel:WORD_1
	global_store_dwordx4 v[72:73], v[66:69], off
	ds_read_b32 v37, v52
	ds_read_b32 v74, v52 offset:1024
	ds_read_b32 v75, v52 offset:2048
	ds_read_b32 v76, v52 offset:3072
	ds_read_b32 v77, v52 offset:4096
	ds_read_b32 v78, v52 offset:5120
	ds_read_b32 v79, v52 offset:6144
	ds_read_b32 v80, v52 offset:7168
	v_add_u32_e32 v66, s8, v51
	v_lshlrev_b32_e32 v67, 1, v66
	v_and_b32_e32 v67, 0xffffffe0, v67
	v_add3_u32 v67, s1, v53, v67
	v_cndmask_b32_e32 v66, v67, v66, vcc
	v_ashrrev_i32_e32 v69, 31, v66
	v_mad_u64_u32 v[66:67], s[2:3], v66, s35, 0
	v_mov_b32_e32 v68, v67
	v_mad_u64_u32 v[68:69], s[2:3], v69, s35, v[68:69]
	v_mov_b32_e32 v67, v68
	v_lshl_add_u64 v[72:73], v[66:67], 1, v[70:71]
	s_waitcnt lgkmcnt(7)
	v_and_b32_sdwa v67, v37, v65 dst_sel:DWORD dst_unused:UNUSED_PAD src0_sel:WORD_1 src1_sel:DWORD
	v_add3_u32 v37, v37, v67, s41
	s_waitcnt lgkmcnt(4)
	v_and_b32_sdwa v67, v76, v65 dst_sel:DWORD dst_unused:UNUSED_PAD src0_sel:WORD_1 src1_sel:DWORD
	v_and_b32_sdwa v68, v74, v65 dst_sel:DWORD dst_unused:UNUSED_PAD src0_sel:WORD_1 src1_sel:DWORD
	v_and_b32_sdwa v66, v75, v65 dst_sel:DWORD dst_unused:UNUSED_PAD src0_sel:WORD_1 src1_sel:DWORD
	v_add3_u32 v67, v76, v67, s41
	v_add3_u32 v68, v74, v68, s41
	v_add3_u32 v66, v75, v66, s41
	v_and_b32_e32 v67, 0xffff0000, v67
	v_and_b32_e32 v68, 0xffff0000, v68
	s_waitcnt lgkmcnt(0)
	v_and_b32_sdwa v69, v80, v65 dst_sel:DWORD dst_unused:UNUSED_PAD src0_sel:WORD_1 src1_sel:DWORD
	v_and_b32_sdwa v74, v78, v65 dst_sel:DWORD dst_unused:UNUSED_PAD src0_sel:WORD_1 src1_sel:DWORD
	v_or_b32_sdwa v67, v67, v66 dst_sel:DWORD dst_unused:UNUSED_PAD src0_sel:DWORD src1_sel:WORD_1
	v_or_b32_sdwa v66, v68, v37 dst_sel:DWORD dst_unused:UNUSED_PAD src0_sel:DWORD src1_sel:WORD_1
	v_and_b32_sdwa v37, v79, v65 dst_sel:DWORD dst_unused:UNUSED_PAD src0_sel:WORD_1 src1_sel:DWORD
	v_and_b32_sdwa v68, v77, v65 dst_sel:DWORD dst_unused:UNUSED_PAD src0_sel:WORD_1 src1_sel:DWORD
	v_add3_u32 v69, v80, v69, s41
	v_add3_u32 v74, v78, v74, s41
	v_add3_u32 v68, v77, v68, s41
	v_add3_u32 v37, v79, v37, s41
	v_and_b32_e32 v69, 0xffff0000, v69
	v_and_b32_e32 v74, 0xffff0000, v74
	v_or_b32_sdwa v69, v69, v37 dst_sel:DWORD dst_unused:UNUSED_PAD src0_sel:DWORD src1_sel:WORD_1
	v_or_b32_sdwa v68, v74, v68 dst_sel:DWORD dst_unused:UNUSED_PAD src0_sel:DWORD src1_sel:WORD_1
	global_store_dwordx4 v[72:73], v[66:69], off
	ds_read_b32 v37, v55
	ds_read_b32 v72, v55 offset:1024
	ds_read_b32 v73, v55 offset:2048
	ds_read_b32 v74, v55 offset:3072
	ds_read_b32 v75, v55 offset:4096
	ds_read_b32 v76, v55 offset:5120
	ds_read_b32 v77, v55 offset:6144
	ds_read_b32 v78, v55 offset:7168
	v_add_u32_e32 v66, s8, v54
	v_lshlrev_b32_e32 v67, 1, v66
	v_and_b32_e32 v67, 0xffffffe0, v67
	v_add3_u32 v67, s1, v56, v67
	v_cndmask_b32_e32 v66, v67, v66, vcc
	v_ashrrev_i32_e32 v69, 31, v66
	v_mad_u64_u32 v[66:67], s[2:3], v66, s35, 0
	v_mov_b32_e32 v68, v67
	v_mad_u64_u32 v[68:69], s[2:3], v69, s35, v[68:69]
	v_mov_b32_e32 v67, v68
	v_lshl_add_u64 v[70:71], v[66:67], 1, v[70:71]
	s_waitcnt lgkmcnt(7)
	v_and_b32_sdwa v67, v37, v65 dst_sel:DWORD dst_unused:UNUSED_PAD src0_sel:WORD_1 src1_sel:DWORD
	v_add3_u32 v37, v37, v67, s41
	s_waitcnt lgkmcnt(4)
	v_and_b32_sdwa v67, v74, v65 dst_sel:DWORD dst_unused:UNUSED_PAD src0_sel:WORD_1 src1_sel:DWORD
	v_and_b32_sdwa v68, v72, v65 dst_sel:DWORD dst_unused:UNUSED_PAD src0_sel:WORD_1 src1_sel:DWORD
	v_and_b32_sdwa v66, v73, v65 dst_sel:DWORD dst_unused:UNUSED_PAD src0_sel:WORD_1 src1_sel:DWORD
	v_add3_u32 v67, v74, v67, s41
	v_add3_u32 v68, v72, v68, s41
	v_add3_u32 v66, v73, v66, s41
	v_and_b32_e32 v67, 0xffff0000, v67
	v_and_b32_e32 v68, 0xffff0000, v68
	s_waitcnt lgkmcnt(0)
	v_and_b32_sdwa v69, v78, v65 dst_sel:DWORD dst_unused:UNUSED_PAD src0_sel:WORD_1 src1_sel:DWORD
	v_and_b32_sdwa v72, v76, v65 dst_sel:DWORD dst_unused:UNUSED_PAD src0_sel:WORD_1 src1_sel:DWORD
	v_or_b32_sdwa v67, v67, v66 dst_sel:DWORD dst_unused:UNUSED_PAD src0_sel:DWORD src1_sel:WORD_1
	v_or_b32_sdwa v66, v68, v37 dst_sel:DWORD dst_unused:UNUSED_PAD src0_sel:DWORD src1_sel:WORD_1
	v_and_b32_sdwa v37, v77, v65 dst_sel:DWORD dst_unused:UNUSED_PAD src0_sel:WORD_1 src1_sel:DWORD
	v_and_b32_sdwa v68, v75, v65 dst_sel:DWORD dst_unused:UNUSED_PAD src0_sel:WORD_1 src1_sel:DWORD
	v_add3_u32 v69, v78, v69, s41
	v_add3_u32 v72, v76, v72, s41
	v_add3_u32 v68, v75, v68, s41
	v_add3_u32 v37, v77, v37, s41
	v_and_b32_e32 v69, 0xffff0000, v69
	v_and_b32_e32 v72, 0xffff0000, v72
	v_or_b32_sdwa v69, v69, v37 dst_sel:DWORD dst_unused:UNUSED_PAD src0_sel:DWORD src1_sel:WORD_1
	v_or_b32_sdwa v68, v72, v68 dst_sel:DWORD dst_unused:UNUSED_PAD src0_sel:DWORD src1_sel:WORD_1
	s_add_i32 s38, s38, s40
	s_add_i32 s39, s39, s40
	s_andn2_b64 vcc, exec, s[22:23]
	s_mov_b32 s1, s43
	s_mov_b32 s21, s10
	s_mov_b32 s8, s26
	s_mov_b32 s20, s30
	s_mov_b32 s35, s42
	s_mov_b64 s[2:3], s[24:25]
	global_store_dwordx4 v[70:71], v[66:69], off
	s_barrier
	s_cbranch_vccz .LBB0_2335
.LBB0_2317:
	s_add_i32 s33, s33, s40
	s_cmp_lt_u32 s34, 2
	s_cselect_b64 s[22:23], -1, 0
	s_and_b64 vcc, exec, s[22:23]
	s_mov_b32 s43, s1
	s_mov_b32 s26, s8
	s_mov_b32 s30, s20
	s_waitcnt vmcnt(0)
	ds_write_b128 v57, v[2:5]
	ds_write_b128 v58, v[6:9]
	ds_write_b128 v59, v[10:13]
	ds_write_b128 v60, v[14:17]
	ds_write_b128 v61, v[18:21]
	ds_write_b128 v62, v[22:25]
	ds_write_b128 v63, v[26:29]
	ds_write_b128 v64, v[30:33]
	s_waitcnt lgkmcnt(0)
	s_barrier
	s_cbranch_vccnz .LBB0_2316
	s_add_i32 s30, s38, 0xa40
	s_cmpk_lt_i32 s30, 0x6c0
	s_cbranch_scc1 .LBB0_2314
	s_cmpk_gt_u32 s30, 0x83f
	s_mov_b64 s[26:27], -1
	s_cbranch_scc0 .LBB0_2332
	s_cmpk_gt_u32 s30, 0x93f
	s_cbranch_scc0 .LBB0_2329
	s_add_i32 s24, s38, 0x100
	s_mul_hi_u32 s10, s39, 0xaaaaaaab
	s_mul_hi_u32 s24, s24, 0xaaaaaaab
	s_lshr_b32 s10, s10, 8
	s_lshr_b32 s26, s24, 8
	s_mulk_i32 s10, 0xfe80
	s_mul_i32 s24, s26, 0xfffffe80
	s_add_i32 s46, s33, s24
	s_add_i32 s45, s38, s10
	s_addk_i32 s46, 0xf6c0
	s_add_i32 s27, s45, 0x100
	s_cmpk_gt_i32 s27, 0x7f
	s_mov_b64 s[30:31], -1
	s_cbranch_scc0 .LBB0_2326
	s_cmpk_gt_u32 s27, 0xff
	s_cbranch_scc0 .LBB0_2324
	s_add_i32 s10, s26, 16
	s_lshl_b64 s[24:25], s[10:11], 23
	s_mov_b32 s27, s11
	s_add_u32 s28, s88, s24
	s_addc_u32 s29, s89, s25
	s_lshl_b64 s[24:25], s[26:27], 22
	s_add_u32 s24, s0, s24
	s_addc_u32 s25, s9, s25
	s_mov_b64 s[30:31], 0

.LBB0_3747:
	s_waitcnt vmcnt(5)
	v_add_u32_e32 v2, 0x800, v34
	s_lshr_b32 s4, s8, 8
	v_ashrrev_i32_e32 v42, 6, v2
	v_cvt_f32_u32_e32 v2, s4
	s_sub_i32 s11, 0, s4
	s_abs_i32 s10, s9
	s_ashr_i32 s5, s9, 31
	v_rcp_iflag_f32_e32 v2, v2
	v_add_u32_e32 v3, 0xa00, v34
	v_ashrrev_i32_e32 v43, 6, v3
	v_add_u32_e32 v3, 0xc00, v34
	v_mul_f32_e32 v2, 0x4f7ffffe, v2
	v_cvt_u32_f32_e32 v2, v2
	v_lshlrev_b32_e32 v1, 2, v34
	v_ashrrev_i32_e32 v44, 6, v3
	v_add_u32_e32 v3, 0xe00, v34
	v_readfirstlane_b32 s12, v2
	s_mul_i32 s11, s11, s12
	s_mul_hi_u32 s11, s12, s11
	s_add_i32 s12, s12, s11
	s_mul_hi_u32 s11, s10, s12
	s_mul_i32 s12, s11, s4
	s_sub_i32 s10, s10, s12
	s_add_i32 s12, s11, 1
	s_sub_i32 s13, s10, s4
	s_cmp_ge_u32 s10, s4
	s_cselect_b32 s11, s12, s11
	s_cselect_b32 s10, s13, s10
	s_add_i32 s12, s11, 1
	s_cmp_ge_u32 s10, s4
	s_cselect_b32 s10, s12, s11
	s_xor_b32 s10, s10, s5
	s_sub_i32 s12, s10, s5
	s_mul_i32 s4, s12, s4
	s_sub_i32 s4, s9, s4
	s_lshl_b32 s4, s4, 8
	s_ashr_i32 s5, s4, 31
	s_lshl_b64 s[10:11], s[4:5], 2
	s_add_u32 s6, s6, s10
	v_and_b32_e32 v38, 0xfc, v1
	v_ashrrev_i32_e32 v45, 6, v3
	s_addc_u32 s7, s7, s11
	s_lshl_b32 s18, s12, 6
	v_mov_b32_e32 v37, 0
	v_lshlrev_b32_e32 v36, 2, v38
	v_add_u32_e32 v2, s18, v45
	v_lshl_add_u64 v[26:27], s[6:7], 0, v[36:37]
	v_ashrrev_i32_e32 v5, 31, v2
	v_mad_u64_u32 v[2:3], s[6:7], v2, s8, 0
	v_mov_b32_e32 v4, v3
	v_mad_u64_u32 v[4:5], s[6:7], v5, s8, v[4:5]
	v_mov_b32_e32 v3, v4
	v_lshl_add_u64 v[10:11], v[2:3], 2, v[26:27]
	v_add_u32_e32 v2, s18, v44
	v_ashrrev_i32_e32 v5, 31, v2
	v_mad_u64_u32 v[2:3], s[6:7], v2, s8, 0
	v_mov_b32_e32 v4, v3
	v_mad_u64_u32 v[4:5], s[6:7], v5, s8, v[4:5]
	v_mov_b32_e32 v3, v4
	v_lshl_add_u64 v[12:13], v[2:3], 2, v[26:27]
	global_load_dwordx4 v[6:9], v[10:11], off
	global_load_dwordx4 v[2:5], v[12:13], off
	v_add_u32_e32 v10, s18, v43
	v_ashrrev_i32_e32 v13, 31, v10
	v_mad_u64_u32 v[10:11], s[6:7], v10, s8, 0
	v_mov_b32_e32 v12, v11
	v_mad_u64_u32 v[12:13], s[6:7], v13, s8, v[12:13]
	v_mov_b32_e32 v11, v12
	v_lshl_add_u64 v[18:19], v[10:11], 2, v[26:27]
	v_add_u32_e32 v10, s18, v42
	v_ashrrev_i32_e32 v13, 31, v10
	v_mad_u64_u32 v[10:11], s[6:7], v10, s8, 0
	v_mov_b32_e32 v12, v11
	v_add_u32_e32 v55, 0x600, v34
	v_mad_u64_u32 v[12:13], s[6:7], v13, s8, v[12:13]
	v_ashrrev_i32_e32 v41, 6, v55
	v_mov_b32_e32 v11, v12
	v_lshl_add_u64 v[20:21], v[10:11], 2, v[26:27]
	global_load_dwordx4 v[14:17], v[18:19], off
	global_load_dwordx4 v[10:13], v[20:21], off
	v_add_u32_e32 v18, s18, v41
	v_ashrrev_i32_e32 v21, 31, v18
	v_mad_u64_u32 v[18:19], s[6:7], v18, s8, 0
	v_mov_b32_e32 v20, v19
	v_add_u32_e32 v52, 0x400, v34
	v_mad_u64_u32 v[20:21], s[6:7], v21, s8, v[20:21]
	v_ashrrev_i32_e32 v40, 6, v52
	v_mov_b32_e32 v19, v20
	v_lshl_add_u64 v[28:29], v[18:19], 2, v[26:27]
	v_add_u32_e32 v18, s18, v40
	v_ashrrev_i32_e32 v21, 31, v18
	v_mad_u64_u32 v[18:19], s[6:7], v18, s8, 0
	v_mov_b32_e32 v20, v19
	v_add_u32_e32 v39, 0x200, v34
	v_mad_u64_u32 v[20:21], s[6:7], v21, s8, v[20:21]
	v_ashrrev_i32_e32 v35, 6, v39
	v_mov_b32_e32 v19, v20
	s_waitcnt vmcnt(8)
	v_lshl_add_u64 v[30:31], v[18:19], 2, v[26:27]
	global_load_dwordx4 v[22:25], v[28:29], off
	global_load_dwordx4 v[18:21], v[30:31], off
	v_add_u32_e32 v28, s18, v35
	v_ashrrev_i32_e32 v31, 31, v28
	v_mad_u64_u32 v[28:29], s[6:7], v28, s8, 0
	v_mov_b32_e32 v30, v29
	v_mad_u64_u32 v[30:31], s[6:7], v31, s8, v[30:31]
	v_ashrrev_i32_e32 v1, 6, v34
	v_mov_b32_e32 v29, v30
	v_lshl_add_u64 v[46:47], v[28:29], 2, v[26:27]
	v_add_u32_e32 v28, s18, v1
	v_ashrrev_i32_e32 v31, 31, v28
	v_mad_u64_u32 v[28:29], s[6:7], v28, s8, 0
	v_mov_b32_e32 v30, v29
	v_mad_u64_u32 v[30:31], s[6:7], v31, s8, v[30:31]
	v_mov_b32_e32 v29, v30
	v_lshl_add_u64 v[48:49], v[28:29], 2, v[26:27]
	global_load_dwordx4 v[30:33], v[46:47], off
	global_load_dwordx4 v[26:29], v[48:49], off
	v_lshlrev_b32_e32 v46, 3, v34
	v_and_b32_e32 v66, 56, v46
	s_movk_i32 s5, 0x400
	v_readlane_b32 s16, v252, 3
	v_mad_u32_u24 v56, v66, s5, 0
	v_mul_lo_u32 v58, v1, s5
	v_mul_lo_u32 v59, v35, s5
	v_mul_lo_u32 v60, v40, s5
	v_mul_lo_u32 v61, v41, s5
	v_mul_lo_u32 v62, v42, s5
	v_mul_lo_u32 v63, v43, s5
	v_mul_lo_u32 v64, v44, s5
	v_mul_lo_u32 v65, v45, s5
	v_readlane_b32 s17, v252, 4
	s_add_u32 s5, s16, 0x1e940000
	s_addc_u32 s30, s17, 0
	s_add_u32 s8, s16, 0x16940000
	s_addc_u32 s9, s17, 0
	s_add_u32 s10, s78, 0x1000000
	s_addc_u32 s11, s79, 0
	s_add_u32 s12, s16, 0x16140000
	s_addc_u32 s13, s17, 0
	v_readlane_b32 s36, v250, 7
	s_add_u32 s31, s16, 0x15540000
	v_readlane_b32 s50, v250, 21
	v_readlane_b32 s51, v250, 22
	s_addc_u32 s33, s17, 0
	s_mov_b64 s[14:15], s[50:51]
	s_add_u32 s14, s14, 0x6c00000
	s_addc_u32 s15, s15, 0
	v_add_u32_e32 v36, 0, v36
	v_ashrrev_i32_e32 v46, 3, v34
	v_ashrrev_i32_e32 v49, 3, v39
	v_ashrrev_i32_e32 v52, 3, v52
	v_ashrrev_i32_e32 v55, 3, v55
	v_readlane_b32 s38, v250, 9
	s_add_u32 s16, s16, 0x11f40000
	s_mov_b32 s7, 0
	v_xor_b32_e32 v48, v46, v66
	v_lshl_add_u32 v47, v48, 2, v56
	v_and_b32_e32 v48, 15, v46
	v_xor_b32_e32 v51, v49, v66
	v_lshl_add_u32 v50, v51, 2, v56
	v_and_b32_e32 v51, 15, v49
	v_xor_b32_e32 v54, v52, v66
	v_lshl_add_u32 v53, v54, 2, v56
	v_and_b32_e32 v54, 15, v52
	v_xor_b32_e32 v57, v55, v66
	v_lshl_add_u32 v56, v57, 2, v56
	v_and_b32_e32 v57, 15, v55
	s_addc_u32 s17, s17, 0
	s_add_i32 s34, s20, 0x15e1
	s_mov_b32 s35, 17
	v_add_u32_e32 v58, v36, v58
	v_add_u32_e32 v59, v36, v59
	v_xor_b32_e32 v59, 32, v59
	v_add_u32_e32 v60, v36, v60
	v_xor_b32_e32 v60, 64, v60
	v_add_u32_e32 v61, v36, v61
	v_xor_b32_e32 v61, 96, v61
	v_add_u32_e32 v62, v36, v62
	v_xor_b32_e32 v62, 128, v62
	v_add_u32_e32 v63, v36, v63
	v_xor_b32_e32 v63, 160, v63
	v_add_u32_e32 v64, v36, v64
	v_xor_b32_e32 v64, 192, v64
	v_add_u32_e32 v65, v36, v65
	v_xor_b32_e32 v65, 224, v65
	v_lshlrev_b32_e32 v36, 2, v38
	v_lshlrev_b32_e32 v38, 1, v66
	s_movk_i32 s36, 0x7fff
	v_mov_b32_e32 v66, 1
	s_mov_b32 s6, s19
	s_mov_b32 s38, s0
	s_mov_b64 s[22:23], s[2:3]
	v_readlane_b32 s37, v250, 8
	v_readlane_b32 s39, v250, 10
	v_readlane_b32 s40, v250, 11
	v_readlane_b32 s41, v250, 12
	v_readlane_b32 s42, v250, 13
	v_readlane_b32 s43, v250, 14
	v_readlane_b32 s44, v250, 15
	v_readlane_b32 s45, v250, 16
	v_readlane_b32 s46, v250, 17
	v_readlane_b32 s47, v250, 18
	v_readlane_b32 s48, v250, 19
	v_readlane_b32 s49, v250, 20
	s_branch .LBB0_3751

.LBB0_3750:
	s_add_i32 s35, s35, -1
	s_cmp_eq_u32 s19, 0
	v_add_u32_e32 v67, s4, v46
	v_lshlrev_b32_e32 v39, 1, v67
	s_cselect_b64 vcc, -1, 0
	s_ashr_i32 s19, s18, 31
	v_and_b32_e32 v39, 0xffffffe0, v39
	s_lshl_b64 s[18:19], s[18:19], 1
	v_add3_u32 v68, s1, v48, v39
	s_add_u32 s2, s2, s18
	s_addc_u32 s3, s3, s19
	v_mov_b32_e32 v39, v37
	v_cndmask_b32_e32 v67, v68, v67, vcc
	v_lshl_add_u64 v[72:73], s[2:3], 0, v[38:39]
	v_mad_u64_u32 v[68:69], s[2:3], v67, s0, 0
	v_ashrrev_i32_e32 v71, 31, v67
	v_mov_b32_e32 v70, v69
	v_mad_u64_u32 v[70:71], s[2:3], v71, s0, v[70:71]
	ds_read_b32 v39, v47
	ds_read_b32 v76, v47 offset:1024
	ds_read_b32 v77, v47 offset:2048
	ds_read_b32 v78, v47 offset:3072
	ds_read_b32 v79, v47 offset:4096
	ds_read_b32 v80, v47 offset:5120
	ds_read_b32 v81, v47 offset:6144
	ds_read_b32 v82, v47 offset:7168
	v_mov_b32_e32 v69, v70
	v_lshl_add_u64 v[74:75], v[68:69], 1, v[72:73]
	s_waitcnt lgkmcnt(7)
	v_and_b32_sdwa v68, v39, v66 dst_sel:DWORD dst_unused:UNUSED_PAD src0_sel:WORD_1 src1_sel:DWORD
	v_add3_u32 v39, v39, v68, s36
	s_waitcnt lgkmcnt(4)
	v_and_b32_sdwa v68, v78, v66 dst_sel:DWORD dst_unused:UNUSED_PAD src0_sel:WORD_1 src1_sel:DWORD
	v_and_b32_sdwa v69, v76, v66 dst_sel:DWORD dst_unused:UNUSED_PAD src0_sel:WORD_1 src1_sel:DWORD
	v_and_b32_sdwa v67, v77, v66 dst_sel:DWORD dst_unused:UNUSED_PAD src0_sel:WORD_1 src1_sel:DWORD
	v_add3_u32 v68, v78, v68, s36
	v_add3_u32 v69, v76, v69, s36
	v_add3_u32 v67, v77, v67, s36
	v_and_b32_e32 v68, 0xffff0000, v68
	v_and_b32_e32 v70, 0xffff0000, v69
	v_or_b32_sdwa v69, v68, v67 dst_sel:DWORD dst_unused:UNUSED_PAD src0_sel:DWORD src1_sel:WORD_1
	v_or_b32_sdwa v68, v70, v39 dst_sel:DWORD dst_unused:UNUSED_PAD src0_sel:DWORD src1_sel:WORD_1
	s_waitcnt lgkmcnt(0)
	v_and_b32_sdwa v70, v82, v66 dst_sel:DWORD dst_unused:UNUSED_PAD src0_sel:WORD_1 src1_sel:DWORD
	v_and_b32_sdwa v71, v80, v66 dst_sel:DWORD dst_unused:UNUSED_PAD src0_sel:WORD_1 src1_sel:DWORD
	v_and_b32_sdwa v39, v81, v66 dst_sel:DWORD dst_unused:UNUSED_PAD src0_sel:WORD_1 src1_sel:DWORD
	v_and_b32_sdwa v67, v79, v66 dst_sel:DWORD dst_unused:UNUSED_PAD src0_sel:WORD_1 src1_sel:DWORD
	v_add3_u32 v70, v82, v70, s36
	v_add3_u32 v71, v80, v71, s36
	v_add3_u32 v67, v79, v67, s36
	v_add3_u32 v39, v81, v39, s36
	v_and_b32_e32 v70, 0xffff0000, v70
	v_and_b32_e32 v76, 0xffff0000, v71
	v_or_b32_sdwa v71, v70, v39 dst_sel:DWORD dst_unused:UNUSED_PAD src0_sel:DWORD src1_sel:WORD_1
	v_or_b32_sdwa v70, v76, v67 dst_sel:DWORD dst_unused:UNUSED_PAD src0_sel:DWORD src1_sel:WORD_1
	global_store_dwordx4 v[74:75], v[68:71], off
	ds_read_b32 v39, v50
	ds_read_b32 v67, v50 offset:1024
	ds_read_b32 v76, v50 offset:2048
	ds_read_b32 v77, v50 offset:3072
	ds_read_b32 v78, v50 offset:4096
	ds_read_b32 v79, v50 offset:5120
	ds_read_b32 v80, v50 offset:6144
	ds_read_b32 v81, v50 offset:7168
	v_add_u32_e32 v68, s4, v49
	v_lshlrev_b32_e32 v69, 1, v68
	v_and_b32_e32 v69, 0xffffffe0, v69
	v_add3_u32 v69, s1, v51, v69
	v_cndmask_b32_e32 v68, v69, v68, vcc
	v_ashrrev_i32_e32 v71, 31, v68
	v_mad_u64_u32 v[68:69], s[2:3], v68, s0, 0
	v_mov_b32_e32 v70, v69
	v_mad_u64_u32 v[70:71], s[2:3], v71, s0, v[70:71]
	v_mov_b32_e32 v69, v70
	v_lshl_add_u64 v[74:75], v[68:69], 1, v[72:73]
	s_waitcnt lgkmcnt(7)
	v_and_b32_sdwa v69, v39, v66 dst_sel:DWORD dst_unused:UNUSED_PAD src0_sel:WORD_1 src1_sel:DWORD
	v_add3_u32 v39, v39, v69, s36
	s_waitcnt lgkmcnt(4)
	v_and_b32_sdwa v69, v77, v66 dst_sel:DWORD dst_unused:UNUSED_PAD src0_sel:WORD_1 src1_sel:DWORD
	v_and_b32_sdwa v70, v67, v66 dst_sel:DWORD dst_unused:UNUSED_PAD src0_sel:WORD_1 src1_sel:DWORD
	v_and_b32_sdwa v68, v76, v66 dst_sel:DWORD dst_unused:UNUSED_PAD src0_sel:WORD_1 src1_sel:DWORD
	v_add3_u32 v69, v77, v69, s36
	v_add3_u32 v67, v67, v70, s36
	v_add3_u32 v68, v76, v68, s36
	v_and_b32_e32 v69, 0xffff0000, v69
	v_and_b32_e32 v67, 0xffff0000, v67
	s_waitcnt lgkmcnt(0)
	v_and_b32_sdwa v70, v81, v66 dst_sel:DWORD dst_unused:UNUSED_PAD src0_sel:WORD_1 src1_sel:DWORD
	v_and_b32_sdwa v71, v79, v66 dst_sel:DWORD dst_unused:UNUSED_PAD src0_sel:WORD_1 src1_sel:DWORD
	v_or_b32_sdwa v69, v69, v68 dst_sel:DWORD dst_unused:UNUSED_PAD src0_sel:DWORD src1_sel:WORD_1
	v_or_b32_sdwa v68, v67, v39 dst_sel:DWORD dst_unused:UNUSED_PAD src0_sel:DWORD src1_sel:WORD_1
	v_and_b32_sdwa v39, v80, v66 dst_sel:DWORD dst_unused:UNUSED_PAD src0_sel:WORD_1 src1_sel:DWORD
	v_and_b32_sdwa v67, v78, v66 dst_sel:DWORD dst_unused:UNUSED_PAD src0_sel:WORD_1 src1_sel:DWORD
	v_add3_u32 v70, v81, v70, s36
	v_add3_u32 v71, v79, v71, s36
	v_add3_u32 v67, v78, v67, s36
	v_add3_u32 v39, v80, v39, s36
	v_and_b32_e32 v70, 0xffff0000, v70
	v_and_b32_e32 v76, 0xffff0000, v71
	v_or_b32_sdwa v71, v70, v39 dst_sel:DWORD dst_unused:UNUSED_PAD src0_sel:DWORD src1_sel:WORD_1
	v_or_b32_sdwa v70, v76, v67 dst_sel:DWORD dst_unused:UNUSED_PAD src0_sel:DWORD src1_sel:WORD_1
	global_store_dwordx4 v[74:75], v[68:71], off
	ds_read_b32 v39, v53
	ds_read_b32 v67, v53 offset:1024
	ds_read_b32 v76, v53 offset:2048
	ds_read_b32 v77, v53 offset:3072
	ds_read_b32 v78, v53 offset:4096
	ds_read_b32 v79, v53 offset:5120
	ds_read_b32 v80, v53 offset:6144
	ds_read_b32 v81, v53 offset:7168
	v_add_u32_e32 v68, s4, v52
	v_lshlrev_b32_e32 v69, 1, v68
	v_and_b32_e32 v69, 0xffffffe0, v69
	v_add3_u32 v69, s1, v54, v69
	v_cndmask_b32_e32 v68, v69, v68, vcc
	v_ashrrev_i32_e32 v71, 31, v68
	v_mad_u64_u32 v[68:69], s[2:3], v68, s0, 0
	v_mov_b32_e32 v70, v69
	v_mad_u64_u32 v[70:71], s[2:3], v71, s0, v[70:71]
	v_mov_b32_e32 v69, v70
	v_lshl_add_u64 v[74:75], v[68:69], 1, v[72:73]
	s_waitcnt lgkmcnt(7)
	v_and_b32_sdwa v69, v39, v66 dst_sel:DWORD dst_unused:UNUSED_PAD src0_sel:WORD_1 src1_sel:DWORD
	v_add3_u32 v39, v39, v69, s36
	s_waitcnt lgkmcnt(4)
	v_and_b32_sdwa v69, v77, v66 dst_sel:DWORD dst_unused:UNUSED_PAD src0_sel:WORD_1 src1_sel:DWORD
	v_and_b32_sdwa v70, v67, v66 dst_sel:DWORD dst_unused:UNUSED_PAD src0_sel:WORD_1 src1_sel:DWORD
	v_and_b32_sdwa v68, v76, v66 dst_sel:DWORD dst_unused:UNUSED_PAD src0_sel:WORD_1 src1_sel:DWORD
	v_add3_u32 v69, v77, v69, s36
	v_add3_u32 v67, v67, v70, s36
	v_add3_u32 v68, v76, v68, s36
	v_and_b32_e32 v69, 0xffff0000, v69
	v_and_b32_e32 v67, 0xffff0000, v67
	s_waitcnt lgkmcnt(0)
	v_and_b32_sdwa v70, v81, v66 dst_sel:DWORD dst_unused:UNUSED_PAD src0_sel:WORD_1 src1_sel:DWORD
	v_and_b32_sdwa v71, v79, v66 dst_sel:DWORD dst_unused:UNUSED_PAD src0_sel:WORD_1 src1_sel:DWORD
	v_or_b32_sdwa v69, v69, v68 dst_sel:DWORD dst_unused:UNUSED_PAD src0_sel:DWORD src1_sel:WORD_1
	v_or_b32_sdwa v68, v67, v39 dst_sel:DWORD dst_unused:UNUSED_PAD src0_sel:DWORD src1_sel:WORD_1
	v_and_b32_sdwa v39, v80, v66 dst_sel:DWORD dst_unused:UNUSED_PAD src0_sel:WORD_1 src1_sel:DWORD
	v_and_b32_sdwa v67, v78, v66 dst_sel:DWORD dst_unused:UNUSED_PAD src0_sel:WORD_1 src1_sel:DWORD
	v_add3_u32 v70, v81, v70, s36
	v_add3_u32 v71, v79, v71, s36
	v_add3_u32 v67, v78, v67, s36
	v_add3_u32 v39, v80, v39, s36
	v_and_b32_e32 v70, 0xffff0000, v70
	v_and_b32_e32 v76, 0xffff0000, v71
	v_or_b32_sdwa v71, v70, v39 dst_sel:DWORD dst_unused:UNUSED_PAD src0_sel:DWORD src1_sel:WORD_1
	v_or_b32_sdwa v70, v76, v67 dst_sel:DWORD dst_unused:UNUSED_PAD src0_sel:DWORD src1_sel:WORD_1
	global_store_dwordx4 v[74:75], v[68:71], off
	ds_read_b32 v39, v56
	ds_read_b32 v67, v56 offset:1024
	ds_read_b32 v74, v56 offset:2048
	ds_read_b32 v75, v56 offset:3072
	ds_read_b32 v76, v56 offset:4096
	ds_read_b32 v77, v56 offset:5120
	ds_read_b32 v78, v56 offset:6144
	ds_read_b32 v79, v56 offset:7168
	v_add_u32_e32 v68, s4, v55
	v_lshlrev_b32_e32 v69, 1, v68
	v_and_b32_e32 v69, 0xffffffe0, v69
	v_add3_u32 v69, s1, v57, v69
	v_cndmask_b32_e32 v68, v69, v68, vcc
	v_ashrrev_i32_e32 v71, 31, v68
	v_mad_u64_u32 v[68:69], s[2:3], v68, s0, 0
	v_mov_b32_e32 v70, v69
	v_mad_u64_u32 v[70:71], s[0:1], v71, s0, v[70:71]
	v_mov_b32_e32 v69, v70
	v_lshl_add_u64 v[72:73], v[68:69], 1, v[72:73]
	s_waitcnt lgkmcnt(7)
	v_and_b32_sdwa v69, v39, v66 dst_sel:DWORD dst_unused:UNUSED_PAD src0_sel:WORD_1 src1_sel:DWORD
	v_add3_u32 v39, v39, v69, s36
	s_waitcnt lgkmcnt(4)
	v_and_b32_sdwa v69, v75, v66 dst_sel:DWORD dst_unused:UNUSED_PAD src0_sel:WORD_1 src1_sel:DWORD
	v_and_b32_sdwa v70, v67, v66 dst_sel:DWORD dst_unused:UNUSED_PAD src0_sel:WORD_1 src1_sel:DWORD
	v_and_b32_sdwa v68, v74, v66 dst_sel:DWORD dst_unused:UNUSED_PAD src0_sel:WORD_1 src1_sel:DWORD
	v_add3_u32 v69, v75, v69, s36
	v_add3_u32 v67, v67, v70, s36
	v_add3_u32 v68, v74, v68, s36
	v_and_b32_e32 v69, 0xffff0000, v69
	v_and_b32_e32 v67, 0xffff0000, v67
	s_waitcnt lgkmcnt(0)
	v_and_b32_sdwa v70, v79, v66 dst_sel:DWORD dst_unused:UNUSED_PAD src0_sel:WORD_1 src1_sel:DWORD
	v_and_b32_sdwa v71, v77, v66 dst_sel:DWORD dst_unused:UNUSED_PAD src0_sel:WORD_1 src1_sel:DWORD
	v_or_b32_sdwa v69, v69, v68 dst_sel:DWORD dst_unused:UNUSED_PAD src0_sel:DWORD src1_sel:WORD_1
	v_or_b32_sdwa v68, v67, v39 dst_sel:DWORD dst_unused:UNUSED_PAD src0_sel:DWORD src1_sel:WORD_1
	v_and_b32_sdwa v39, v78, v66 dst_sel:DWORD dst_unused:UNUSED_PAD src0_sel:WORD_1 src1_sel:DWORD
	v_and_b32_sdwa v67, v76, v66 dst_sel:DWORD dst_unused:UNUSED_PAD src0_sel:WORD_1 src1_sel:DWORD
	v_add3_u32 v70, v79, v70, s36
	v_add3_u32 v71, v77, v71, s36
	v_add3_u32 v67, v76, v67, s36
	v_add3_u32 v39, v78, v39, s36
	v_and_b32_e32 v70, 0xffff0000, v70
	v_and_b32_e32 v74, 0xffff0000, v71
	v_or_b32_sdwa v71, v70, v39 dst_sel:DWORD dst_unused:UNUSED_PAD src0_sel:DWORD src1_sel:WORD_1
	v_or_b32_sdwa v70, v74, v67 dst_sel:DWORD dst_unused:UNUSED_PAD src0_sel:DWORD src1_sel:WORD_1
	s_add_i32 s34, s34, 1
	s_and_b64 vcc, exec, s[20:21]
	s_mov_b32 s28, s37
	s_mov_b32 s1, s39
	s_mov_b32 s19, s6
	s_mov_b32 s4, s24
	s_mov_b32 s18, s29
	s_mov_b32 s0, s38
	s_mov_b64 s[2:3], s[22:23]
	global_store_dwordx4 v[72:73], v[68:71], off
	s_barrier
	s_cbranch_vccnz .LBB0_3769
.LBB0_3751:
	s_add_i32 s37, s28, 1
	s_cmp_lt_u32 s35, 2
	s_cselect_b64 s[20:21], -1, 0
	s_and_b64 vcc, exec, s[20:21]
	s_mov_b32 s39, s1
	s_mov_b32 s24, s4
	s_mov_b32 s29, s18
	s_waitcnt vmcnt(0)
	ds_write_b128 v58, v[26:29]
	ds_write_b128 v59, v[30:33]
	ds_write_b128 v60, v[18:21]
	ds_write_b128 v61, v[22:25]
	ds_write_b128 v62, v[10:13]
	ds_write_b128 v63, v[14:17]
	ds_write_b128 v64, v[2:5]
	ds_write_b128 v65, v[6:9]
	s_waitcnt lgkmcnt(0)
	s_barrier
	s_cbranch_vccnz .LBB0_3750
	s_add_i32 s6, s34, 0x93f
	s_cmpk_lt_i32 s6, 0x6bf
	s_cbranch_scc1 .LBB0_3748
	s_add_i32 s29, s34, 0x940
	s_cmpk_gt_u32 s29, 0x83f
	s_mov_b64 s[24:25], -1
	s_cbranch_scc0 .LBB0_3766
	s_cmpk_gt_u32 s29, 0x93f
	s_cbranch_scc0 .LBB0_3763
	s_mul_hi_u32 s6, s34, 0xaaaaaaab
	s_lshr_b32 s24, s6, 8
	s_mul_i32 s6, s24, 0xfffffe80
	s_add_i32 s42, s28, s6
	s_addk_i32 s42, 0xf6c1
	s_add_i32 s25, s34, s6
	s_cmpk_gt_i32 s25, 0x7f
	s_mov_b64 s[28:29], -1
	s_cbranch_scc0 .LBB0_3760
	s_cmpk_gt_u32 s25, 0xff
	s_cbranch_scc0 .LBB0_3758
	s_add_i32 s6, s24, 16
	s_add_i32 s41, s42, 0xffffff00
	s_lshl_b64 s[22:23], s[6:7], 23
	s_mov_b32 s25, s7
	s_add_u32 s26, s88, s22
	s_addc_u32 s27, s89, s23
	s_lshl_b64 s[22:23], s[24:25], 22
	s_add_u32 s22, s5, s22
	s_addc_u32 s23, s30, s23
	s_mov_b64 s[28:29], 0

.LBB0_3796:
	s_waitcnt vmcnt(5)
	v_add_u32_e32 v2, 0x800, v34
	s_lshr_b32 s0, s8, 8
	v_ashrrev_i32_e32 v42, 6, v2
	v_cvt_f32_u32_e32 v2, s0
	s_sub_i32 s10, 0, s0
	s_abs_i32 s5, s9
	s_ashr_i32 s4, s9, 31
	v_rcp_iflag_f32_e32 v2, v2
	v_add_u32_e32 v3, 0xa00, v34
	v_ashrrev_i32_e32 v43, 6, v3
	v_add_u32_e32 v3, 0xc00, v34
	v_mul_f32_e32 v2, 0x4f7ffffe, v2
	v_cvt_u32_f32_e32 v2, v2
	v_lshlrev_b32_e32 v1, 2, v34
	v_ashrrev_i32_e32 v44, 6, v3
	v_add_u32_e32 v3, 0xe00, v34
	v_readfirstlane_b32 s11, v2
	s_mul_i32 s10, s10, s11
	s_mul_hi_u32 s10, s11, s10
	s_add_i32 s11, s11, s10
	s_mul_hi_u32 s10, s5, s11
	s_mul_i32 s11, s10, s0
	s_sub_i32 s5, s5, s11
	s_add_i32 s11, s10, 1
	s_sub_i32 s12, s5, s0
	s_cmp_ge_u32 s5, s0
	s_cselect_b32 s10, s11, s10
	s_cselect_b32 s5, s12, s5
	s_add_i32 s11, s10, 1
	s_cmp_ge_u32 s5, s0
	s_cselect_b32 s5, s11, s10
	s_xor_b32 s5, s5, s4
	s_sub_i32 s12, s5, s4
	s_mul_i32 s0, s12, s0
	s_sub_i32 s0, s9, s0
	s_lshl_b32 s4, s0, 8
	s_ashr_i32 s5, s4, 31
	s_lshl_b64 s[10:11], s[4:5], 2
	s_add_u32 s6, s6, s10
	v_and_b32_e32 v38, 0xfc, v1
	v_ashrrev_i32_e32 v45, 6, v3
	s_addc_u32 s7, s7, s11
	s_lshl_b32 s18, s12, 6
	v_mov_b32_e32 v37, 0
	v_lshlrev_b32_e32 v36, 2, v38
	v_add_u32_e32 v2, s18, v45
	v_lshl_add_u64 v[26:27], s[6:7], 0, v[36:37]
	v_ashrrev_i32_e32 v5, 31, v2
	v_mad_u64_u32 v[2:3], s[6:7], v2, s8, 0
	v_mov_b32_e32 v4, v3
	v_mad_u64_u32 v[4:5], s[6:7], v5, s8, v[4:5]
	v_mov_b32_e32 v3, v4
	v_lshl_add_u64 v[10:11], v[2:3], 2, v[26:27]
	v_add_u32_e32 v2, s18, v44
	v_ashrrev_i32_e32 v5, 31, v2
	v_mad_u64_u32 v[2:3], s[6:7], v2, s8, 0
	v_mov_b32_e32 v4, v3
	v_mad_u64_u32 v[4:5], s[6:7], v5, s8, v[4:5]
	v_mov_b32_e32 v3, v4
	v_lshl_add_u64 v[12:13], v[2:3], 2, v[26:27]
	global_load_dwordx4 v[6:9], v[10:11], off
	global_load_dwordx4 v[2:5], v[12:13], off
	v_add_u32_e32 v10, s18, v43
	v_ashrrev_i32_e32 v13, 31, v10
	v_mad_u64_u32 v[10:11], s[6:7], v10, s8, 0
	v_mov_b32_e32 v12, v11
	v_mad_u64_u32 v[12:13], s[6:7], v13, s8, v[12:13]
	v_mov_b32_e32 v11, v12
	v_lshl_add_u64 v[18:19], v[10:11], 2, v[26:27]
	v_add_u32_e32 v10, s18, v42
	v_ashrrev_i32_e32 v13, 31, v10
	v_mad_u64_u32 v[10:11], s[6:7], v10, s8, 0
	v_mov_b32_e32 v12, v11
	v_add_u32_e32 v55, 0x600, v34
	v_mad_u64_u32 v[12:13], s[6:7], v13, s8, v[12:13]
	v_ashrrev_i32_e32 v41, 6, v55
	v_mov_b32_e32 v11, v12
	v_lshl_add_u64 v[20:21], v[10:11], 2, v[26:27]
	global_load_dwordx4 v[14:17], v[18:19], off
	global_load_dwordx4 v[10:13], v[20:21], off
	v_add_u32_e32 v18, s18, v41
	v_ashrrev_i32_e32 v21, 31, v18
	v_mad_u64_u32 v[18:19], s[6:7], v18, s8, 0
	v_mov_b32_e32 v20, v19
	v_add_u32_e32 v52, 0x400, v34
	v_mad_u64_u32 v[20:21], s[6:7], v21, s8, v[20:21]
	v_ashrrev_i32_e32 v40, 6, v52
	v_mov_b32_e32 v19, v20
	v_lshl_add_u64 v[28:29], v[18:19], 2, v[26:27]
	v_add_u32_e32 v18, s18, v40
	v_ashrrev_i32_e32 v21, 31, v18
	v_mad_u64_u32 v[18:19], s[6:7], v18, s8, 0
	v_mov_b32_e32 v20, v19
	v_add_u32_e32 v35, 0x200, v34
	v_mad_u64_u32 v[20:21], s[6:7], v21, s8, v[20:21]
	v_ashrrev_i32_e32 v39, 6, v35
	v_mov_b32_e32 v19, v20
	s_waitcnt vmcnt(8)
	v_lshl_add_u64 v[30:31], v[18:19], 2, v[26:27]
	global_load_dwordx4 v[22:25], v[28:29], off
	global_load_dwordx4 v[18:21], v[30:31], off
	v_add_u32_e32 v28, s18, v39
	v_ashrrev_i32_e32 v31, 31, v28
	v_mad_u64_u32 v[28:29], s[6:7], v28, s8, 0
	v_mov_b32_e32 v30, v29
	v_mad_u64_u32 v[30:31], s[6:7], v31, s8, v[30:31]
	v_ashrrev_i32_e32 v1, 6, v34
	v_mov_b32_e32 v29, v30
	v_lshl_add_u64 v[46:47], v[28:29], 2, v[26:27]
	v_add_u32_e32 v28, s18, v1
	v_ashrrev_i32_e32 v31, 31, v28
	v_mad_u64_u32 v[28:29], s[6:7], v28, s8, 0
	v_mov_b32_e32 v30, v29
	v_mad_u64_u32 v[30:31], s[6:7], v31, s8, v[30:31]
	v_mov_b32_e32 v29, v30
	v_lshl_add_u64 v[48:49], v[28:29], 2, v[26:27]
	global_load_dwordx4 v[30:33], v[46:47], off
	global_load_dwordx4 v[26:29], v[48:49], off
	v_lshlrev_b32_e32 v46, 3, v34
	v_and_b32_e32 v66, 56, v46
	s_movk_i32 s0, 0x400
	v_readlane_b32 s16, v252, 3
	v_mad_u32_u24 v56, v66, s0, 0
	v_mul_lo_u32 v58, v1, s0
	v_mul_lo_u32 v59, v39, s0
	v_mul_lo_u32 v60, v40, s0
	v_mul_lo_u32 v61, v41, s0
	v_mul_lo_u32 v62, v42, s0
	v_mul_lo_u32 v63, v43, s0
	v_mul_lo_u32 v64, v44, s0
	v_mul_lo_u32 v65, v45, s0
	v_readlane_b32 s17, v252, 4
	s_add_u32 s0, s16, 0x1e940000
	s_addc_u32 s5, s17, 0
	s_add_u32 s8, s16, 0x16940000
	s_addc_u32 s9, s17, 0
	s_add_u32 s10, s78, 0x1000000
	s_addc_u32 s11, s79, 0
	s_add_u32 s12, s16, 0x16140000
	s_addc_u32 s13, s17, 0
	v_readlane_b32 s36, v250, 7
	s_add_u32 s31, s16, 0x15540000
	v_readlane_b32 s50, v250, 21
	v_readlane_b32 s51, v250, 22
	s_addc_u32 s33, s17, 0
	s_mov_b64 s[14:15], s[50:51]
	s_add_u32 s14, s14, 0x6c00000
	s_addc_u32 s15, s15, 0
	v_add_u32_e32 v36, 0, v36
	v_ashrrev_i32_e32 v46, 3, v34
	v_ashrrev_i32_e32 v49, 3, v35
	v_ashrrev_i32_e32 v52, 3, v52
	v_ashrrev_i32_e32 v55, 3, v55
	v_readlane_b32 s38, v250, 9
	s_add_u32 s16, s16, 0x11f40000
	s_mov_b32 s7, 0
	v_xor_b32_e32 v48, v46, v66
	v_lshl_add_u32 v47, v48, 2, v56
	v_and_b32_e32 v48, 15, v46
	v_xor_b32_e32 v51, v49, v66
	v_lshl_add_u32 v50, v51, 2, v56
	v_and_b32_e32 v51, 15, v49
	v_xor_b32_e32 v54, v52, v66
	v_lshl_add_u32 v53, v54, 2, v56
	v_and_b32_e32 v54, 15, v52
	v_xor_b32_e32 v57, v55, v66
	v_lshl_add_u32 v56, v57, 2, v56
	v_and_b32_e32 v57, 15, v55
	s_addc_u32 s17, s17, 0
	s_add_i32 s34, s20, 0xfffffce1
	s_mov_b32 s35, 25
	v_add_u32_e32 v58, v36, v58
	v_add_u32_e32 v59, v36, v59
	v_xor_b32_e32 v59, 32, v59
	v_add_u32_e32 v60, v36, v60
	v_xor_b32_e32 v60, 64, v60
	v_add_u32_e32 v61, v36, v61
	v_xor_b32_e32 v61, 96, v61
	v_add_u32_e32 v62, v36, v62
	v_xor_b32_e32 v62, 128, v62
	v_add_u32_e32 v63, v36, v63
	v_xor_b32_e32 v63, 160, v63
	v_add_u32_e32 v64, v36, v64
	v_xor_b32_e32 v64, 192, v64
	v_add_u32_e32 v65, v36, v65
	v_xor_b32_e32 v65, 224, v65
	v_lshlrev_b32_e32 v36, 2, v38
	v_lshlrev_b32_e32 v34, 1, v66
	s_movk_i32 s36, 0x7fff
	v_mov_b32_e32 v38, 1
	s_mov_b32 s6, s19
	s_mov_b32 s38, s30
	s_mov_b64 s[22:23], s[2:3]
	v_readlane_b32 s37, v250, 8
	v_readlane_b32 s39, v250, 10
	v_readlane_b32 s40, v250, 11
	v_readlane_b32 s41, v250, 12
	v_readlane_b32 s42, v250, 13
	v_readlane_b32 s43, v250, 14
	v_readlane_b32 s44, v250, 15
	v_readlane_b32 s45, v250, 16
	v_readlane_b32 s46, v250, 17
	v_readlane_b32 s47, v250, 18
	v_readlane_b32 s48, v250, 19
	v_readlane_b32 s49, v250, 20
	s_branch .LBB0_3800

.LBB0_3799:
	s_add_i32 s35, s35, -1
	s_cmp_eq_u32 s19, 0
	v_add_u32_e32 v66, s4, v46
	v_lshlrev_b32_e32 v35, 1, v66
	s_cselect_b64 vcc, -1, 0
	s_ashr_i32 s19, s18, 31
	v_and_b32_e32 v35, 0xffffffe0, v35
	s_lshl_b64 s[18:19], s[18:19], 1
	v_add3_u32 v67, s1, v48, v35
	s_add_u32 s2, s2, s18
	s_addc_u32 s3, s3, s19
	v_mov_b32_e32 v35, v37
	v_cndmask_b32_e32 v66, v67, v66, vcc
	v_lshl_add_u64 v[70:71], s[2:3], 0, v[34:35]
	v_ashrrev_i32_e32 v69, 31, v66
	v_mad_u64_u32 v[66:67], s[2:3], v66, s30, 0
	v_mov_b32_e32 v68, v67
	ds_read_b32 v35, v47
	ds_read_b32 v74, v47 offset:1024
	ds_read_b32 v75, v47 offset:2048
	ds_read_b32 v76, v47 offset:3072
	ds_read_b32 v77, v47 offset:4096
	ds_read_b32 v78, v47 offset:5120
	ds_read_b32 v79, v47 offset:6144
	ds_read_b32 v80, v47 offset:7168
	v_mad_u64_u32 v[68:69], s[2:3], v69, s30, v[68:69]
	v_mov_b32_e32 v67, v68
	v_lshl_add_u64 v[72:73], v[66:67], 1, v[70:71]
	s_waitcnt lgkmcnt(7)
	v_and_b32_sdwa v67, v35, v38 dst_sel:DWORD dst_unused:UNUSED_PAD src0_sel:WORD_1 src1_sel:DWORD
	v_add3_u32 v35, v35, v67, s36
	s_waitcnt lgkmcnt(4)
	v_and_b32_sdwa v67, v76, v38 dst_sel:DWORD dst_unused:UNUSED_PAD src0_sel:WORD_1 src1_sel:DWORD
	v_and_b32_sdwa v68, v74, v38 dst_sel:DWORD dst_unused:UNUSED_PAD src0_sel:WORD_1 src1_sel:DWORD
	v_and_b32_sdwa v66, v75, v38 dst_sel:DWORD dst_unused:UNUSED_PAD src0_sel:WORD_1 src1_sel:DWORD
	v_add3_u32 v67, v76, v67, s36
	v_add3_u32 v68, v74, v68, s36
	v_add3_u32 v66, v75, v66, s36
	v_and_b32_e32 v67, 0xffff0000, v67
	v_and_b32_e32 v68, 0xffff0000, v68
	s_waitcnt lgkmcnt(0)
	v_and_b32_sdwa v69, v80, v38 dst_sel:DWORD dst_unused:UNUSED_PAD src0_sel:WORD_1 src1_sel:DWORD
	v_and_b32_sdwa v74, v78, v38 dst_sel:DWORD dst_unused:UNUSED_PAD src0_sel:WORD_1 src1_sel:DWORD
	v_or_b32_sdwa v67, v67, v66 dst_sel:DWORD dst_unused:UNUSED_PAD src0_sel:DWORD src1_sel:WORD_1
	v_or_b32_sdwa v66, v68, v35 dst_sel:DWORD dst_unused:UNUSED_PAD src0_sel:DWORD src1_sel:WORD_1
	v_and_b32_sdwa v35, v79, v38 dst_sel:DWORD dst_unused:UNUSED_PAD src0_sel:WORD_1 src1_sel:DWORD
	v_and_b32_sdwa v68, v77, v38 dst_sel:DWORD dst_unused:UNUSED_PAD src0_sel:WORD_1 src1_sel:DWORD
	v_add3_u32 v69, v80, v69, s36
	v_add3_u32 v74, v78, v74, s36
	v_add3_u32 v68, v77, v68, s36
	v_add3_u32 v35, v79, v35, s36
	v_and_b32_e32 v69, 0xffff0000, v69
	v_and_b32_e32 v74, 0xffff0000, v74
	v_or_b32_sdwa v69, v69, v35 dst_sel:DWORD dst_unused:UNUSED_PAD src0_sel:DWORD src1_sel:WORD_1
	v_or_b32_sdwa v68, v74, v68 dst_sel:DWORD dst_unused:UNUSED_PAD src0_sel:DWORD src1_sel:WORD_1
	global_store_dwordx4 v[72:73], v[66:69], off
	ds_read_b32 v35, v50
	ds_read_b32 v74, v50 offset:1024
	ds_read_b32 v75, v50 offset:2048
	ds_read_b32 v76, v50 offset:3072
	ds_read_b32 v77, v50 offset:4096
	ds_read_b32 v78, v50 offset:5120
	ds_read_b32 v79, v50 offset:6144
	ds_read_b32 v80, v50 offset:7168
	v_add_u32_e32 v66, s4, v49
	v_lshlrev_b32_e32 v67, 1, v66
	v_and_b32_e32 v67, 0xffffffe0, v67
	v_add3_u32 v67, s1, v51, v67
	v_cndmask_b32_e32 v66, v67, v66, vcc
	v_ashrrev_i32_e32 v69, 31, v66
	v_mad_u64_u32 v[66:67], s[2:3], v66, s30, 0
	v_mov_b32_e32 v68, v67
	v_mad_u64_u32 v[68:69], s[2:3], v69, s30, v[68:69]
	v_mov_b32_e32 v67, v68
	v_lshl_add_u64 v[72:73], v[66:67], 1, v[70:71]
	s_waitcnt lgkmcnt(7)
	v_and_b32_sdwa v67, v35, v38 dst_sel:DWORD dst_unused:UNUSED_PAD src0_sel:WORD_1 src1_sel:DWORD
	v_add3_u32 v35, v35, v67, s36
	s_waitcnt lgkmcnt(4)
	v_and_b32_sdwa v67, v76, v38 dst_sel:DWORD dst_unused:UNUSED_PAD src0_sel:WORD_1 src1_sel:DWORD
	v_and_b32_sdwa v68, v74, v38 dst_sel:DWORD dst_unused:UNUSED_PAD src0_sel:WORD_1 src1_sel:DWORD
	v_and_b32_sdwa v66, v75, v38 dst_sel:DWORD dst_unused:UNUSED_PAD src0_sel:WORD_1 src1_sel:DWORD
	v_add3_u32 v67, v76, v67, s36
	v_add3_u32 v68, v74, v68, s36
	v_add3_u32 v66, v75, v66, s36
	v_and_b32_e32 v67, 0xffff0000, v67
	v_and_b32_e32 v68, 0xffff0000, v68
	s_waitcnt lgkmcnt(0)
	v_and_b32_sdwa v69, v80, v38 dst_sel:DWORD dst_unused:UNUSED_PAD src0_sel:WORD_1 src1_sel:DWORD
	v_and_b32_sdwa v74, v78, v38 dst_sel:DWORD dst_unused:UNUSED_PAD src0_sel:WORD_1 src1_sel:DWORD
	v_or_b32_sdwa v67, v67, v66 dst_sel:DWORD dst_unused:UNUSED_PAD src0_sel:DWORD src1_sel:WORD_1
	v_or_b32_sdwa v66, v68, v35 dst_sel:DWORD dst_unused:UNUSED_PAD src0_sel:DWORD src1_sel:WORD_1
	v_and_b32_sdwa v35, v79, v38 dst_sel:DWORD dst_unused:UNUSED_PAD src0_sel:WORD_1 src1_sel:DWORD
	v_and_b32_sdwa v68, v77, v38 dst_sel:DWORD dst_unused:UNUSED_PAD src0_sel:WORD_1 src1_sel:DWORD
	v_add3_u32 v69, v80, v69, s36
	v_add3_u32 v74, v78, v74, s36
	v_add3_u32 v68, v77, v68, s36
	v_add3_u32 v35, v79, v35, s36
	v_and_b32_e32 v69, 0xffff0000, v69
	v_and_b32_e32 v74, 0xffff0000, v74
	v_or_b32_sdwa v69, v69, v35 dst_sel:DWORD dst_unused:UNUSED_PAD src0_sel:DWORD src1_sel:WORD_1
	v_or_b32_sdwa v68, v74, v68 dst_sel:DWORD dst_unused:UNUSED_PAD src0_sel:DWORD src1_sel:WORD_1
	global_store_dwordx4 v[72:73], v[66:69], off
	ds_read_b32 v35, v53
	ds_read_b32 v74, v53 offset:1024
	ds_read_b32 v75, v53 offset:2048
	ds_read_b32 v76, v53 offset:3072
	ds_read_b32 v77, v53 offset:4096
	ds_read_b32 v78, v53 offset:5120
	ds_read_b32 v79, v53 offset:6144
	ds_read_b32 v80, v53 offset:7168
	v_add_u32_e32 v66, s4, v52
	v_lshlrev_b32_e32 v67, 1, v66
	v_and_b32_e32 v67, 0xffffffe0, v67
	v_add3_u32 v67, s1, v54, v67
	v_cndmask_b32_e32 v66, v67, v66, vcc
	v_ashrrev_i32_e32 v69, 31, v66
	v_mad_u64_u32 v[66:67], s[2:3], v66, s30, 0
	v_mov_b32_e32 v68, v67
	v_mad_u64_u32 v[68:69], s[2:3], v69, s30, v[68:69]
	v_mov_b32_e32 v67, v68
	v_lshl_add_u64 v[72:73], v[66:67], 1, v[70:71]
	s_waitcnt lgkmcnt(7)
	v_and_b32_sdwa v67, v35, v38 dst_sel:DWORD dst_unused:UNUSED_PAD src0_sel:WORD_1 src1_sel:DWORD
	v_add3_u32 v35, v35, v67, s36
	s_waitcnt lgkmcnt(4)
	v_and_b32_sdwa v67, v76, v38 dst_sel:DWORD dst_unused:UNUSED_PAD src0_sel:WORD_1 src1_sel:DWORD
	v_and_b32_sdwa v68, v74, v38 dst_sel:DWORD dst_unused:UNUSED_PAD src0_sel:WORD_1 src1_sel:DWORD
	v_and_b32_sdwa v66, v75, v38 dst_sel:DWORD dst_unused:UNUSED_PAD src0_sel:WORD_1 src1_sel:DWORD
	v_add3_u32 v67, v76, v67, s36
	v_add3_u32 v68, v74, v68, s36
	v_add3_u32 v66, v75, v66, s36
	v_and_b32_e32 v67, 0xffff0000, v67
	v_and_b32_e32 v68, 0xffff0000, v68
	s_waitcnt lgkmcnt(0)
	v_and_b32_sdwa v69, v80, v38 dst_sel:DWORD dst_unused:UNUSED_PAD src0_sel:WORD_1 src1_sel:DWORD
	v_and_b32_sdwa v74, v78, v38 dst_sel:DWORD dst_unused:UNUSED_PAD src0_sel:WORD_1 src1_sel:DWORD
	v_or_b32_sdwa v67, v67, v66 dst_sel:DWORD dst_unused:UNUSED_PAD src0_sel:DWORD src1_sel:WORD_1
	v_or_b32_sdwa v66, v68, v35 dst_sel:DWORD dst_unused:UNUSED_PAD src0_sel:DWORD src1_sel:WORD_1
	v_and_b32_sdwa v35, v79, v38 dst_sel:DWORD dst_unused:UNUSED_PAD src0_sel:WORD_1 src1_sel:DWORD
	v_and_b32_sdwa v68, v77, v38 dst_sel:DWORD dst_unused:UNUSED_PAD src0_sel:WORD_1 src1_sel:DWORD
	v_add3_u32 v69, v80, v69, s36
	v_add3_u32 v74, v78, v74, s36
	v_add3_u32 v68, v77, v68, s36
	v_add3_u32 v35, v79, v35, s36
	v_and_b32_e32 v69, 0xffff0000, v69
	v_and_b32_e32 v74, 0xffff0000, v74
	v_or_b32_sdwa v69, v69, v35 dst_sel:DWORD dst_unused:UNUSED_PAD src0_sel:DWORD src1_sel:WORD_1
	v_or_b32_sdwa v68, v74, v68 dst_sel:DWORD dst_unused:UNUSED_PAD src0_sel:DWORD src1_sel:WORD_1
	global_store_dwordx4 v[72:73], v[66:69], off
	ds_read_b32 v35, v56
	ds_read_b32 v72, v56 offset:1024
	ds_read_b32 v73, v56 offset:2048
	ds_read_b32 v74, v56 offset:3072
	ds_read_b32 v75, v56 offset:4096
	ds_read_b32 v76, v56 offset:5120
	ds_read_b32 v77, v56 offset:6144
	ds_read_b32 v78, v56 offset:7168
	v_add_u32_e32 v66, s4, v55
	v_lshlrev_b32_e32 v67, 1, v66
	v_and_b32_e32 v67, 0xffffffe0, v67
	v_add3_u32 v67, s1, v57, v67
	v_cndmask_b32_e32 v66, v67, v66, vcc
	v_ashrrev_i32_e32 v69, 31, v66
	v_mad_u64_u32 v[66:67], s[2:3], v66, s30, 0
	v_mov_b32_e32 v68, v67
	v_mad_u64_u32 v[68:69], s[2:3], v69, s30, v[68:69]
	v_mov_b32_e32 v67, v68
	v_lshl_add_u64 v[70:71], v[66:67], 1, v[70:71]
	s_waitcnt lgkmcnt(7)
	v_and_b32_sdwa v67, v35, v38 dst_sel:DWORD dst_unused:UNUSED_PAD src0_sel:WORD_1 src1_sel:DWORD
	v_add3_u32 v35, v35, v67, s36
	s_waitcnt lgkmcnt(4)
	v_and_b32_sdwa v67, v74, v38 dst_sel:DWORD dst_unused:UNUSED_PAD src0_sel:WORD_1 src1_sel:DWORD
	v_and_b32_sdwa v68, v72, v38 dst_sel:DWORD dst_unused:UNUSED_PAD src0_sel:WORD_1 src1_sel:DWORD
	v_and_b32_sdwa v66, v73, v38 dst_sel:DWORD dst_unused:UNUSED_PAD src0_sel:WORD_1 src1_sel:DWORD
	v_add3_u32 v67, v74, v67, s36
	v_add3_u32 v68, v72, v68, s36
	v_add3_u32 v66, v73, v66, s36
	v_and_b32_e32 v67, 0xffff0000, v67
	v_and_b32_e32 v68, 0xffff0000, v68
	s_waitcnt lgkmcnt(0)
	v_and_b32_sdwa v69, v78, v38 dst_sel:DWORD dst_unused:UNUSED_PAD src0_sel:WORD_1 src1_sel:DWORD
	v_and_b32_sdwa v72, v76, v38 dst_sel:DWORD dst_unused:UNUSED_PAD src0_sel:WORD_1 src1_sel:DWORD
	v_or_b32_sdwa v67, v67, v66 dst_sel:DWORD dst_unused:UNUSED_PAD src0_sel:DWORD src1_sel:WORD_1
	v_or_b32_sdwa v66, v68, v35 dst_sel:DWORD dst_unused:UNUSED_PAD src0_sel:DWORD src1_sel:WORD_1
	v_and_b32_sdwa v35, v77, v38 dst_sel:DWORD dst_unused:UNUSED_PAD src0_sel:WORD_1 src1_sel:DWORD
	v_and_b32_sdwa v68, v75, v38 dst_sel:DWORD dst_unused:UNUSED_PAD src0_sel:WORD_1 src1_sel:DWORD
	v_add3_u32 v69, v78, v69, s36
	v_add3_u32 v72, v76, v72, s36
	v_add3_u32 v68, v75, v68, s36
	v_add3_u32 v35, v77, v35, s36
	v_and_b32_e32 v69, 0xffff0000, v69
	v_and_b32_e32 v72, 0xffff0000, v72
	v_or_b32_sdwa v69, v69, v35 dst_sel:DWORD dst_unused:UNUSED_PAD src0_sel:DWORD src1_sel:WORD_1
	v_or_b32_sdwa v68, v72, v68 dst_sel:DWORD dst_unused:UNUSED_PAD src0_sel:DWORD src1_sel:WORD_1
	s_add_i32 s34, s34, 1
	s_and_b64 vcc, exec, s[20:21]
	s_mov_b32 s28, s37
	s_mov_b32 s1, s39
	s_mov_b32 s19, s6
	s_mov_b32 s4, s24
	s_mov_b32 s18, s29
	s_mov_b32 s30, s38
	s_mov_b64 s[2:3], s[22:23]
	global_store_dwordx4 v[70:71], v[66:69], off
	s_barrier
	s_cbranch_vccnz .LBB0_3818
.LBB0_3800:
	s_add_i32 s37, s28, 1
	s_cmp_lt_u32 s35, 2
	s_cselect_b64 s[20:21], -1, 0
	s_and_b64 vcc, exec, s[20:21]
	s_mov_b32 s39, s1
	s_mov_b32 s24, s4
	s_mov_b32 s29, s18
	s_waitcnt vmcnt(0)
	ds_write_b128 v58, v[26:29]
	ds_write_b128 v59, v[30:33]
	ds_write_b128 v60, v[18:21]
	ds_write_b128 v61, v[22:25]
	ds_write_b128 v62, v[10:13]
	ds_write_b128 v63, v[14:17]
	ds_write_b128 v64, v[2:5]
	ds_write_b128 v65, v[6:9]
	s_waitcnt lgkmcnt(0)
	s_barrier
	s_cbranch_vccnz .LBB0_3799
	s_add_i32 s6, s34, 0x93f
	s_cmpk_lt_i32 s6, 0x6bf
	s_cbranch_scc1 .LBB0_3797
	s_add_i32 s29, s34, 0x940
	s_cmpk_gt_u32 s29, 0x83f
	s_mov_b64 s[24:25], -1
	s_cbranch_scc0 .LBB0_3815
	s_cmpk_gt_u32 s29, 0x93f
	s_cbranch_scc0 .LBB0_3812
	s_mul_hi_u32 s6, s34, 0xaaaaaaab
	s_lshr_b32 s24, s6, 8
	s_mul_i32 s6, s24, 0xfffffe80
	s_add_i32 s42, s28, s6
	s_addk_i32 s42, 0xf6c1
	s_add_i32 s25, s34, s6
	s_cmpk_gt_i32 s25, 0x7f
	s_mov_b64 s[28:29], -1
	s_cbranch_scc0 .LBB0_3809
	s_cmpk_gt_u32 s25, 0xff
	s_cbranch_scc0 .LBB0_3807
	s_add_i32 s6, s24, 16
	s_add_i32 s41, s42, 0xffffff00
	s_lshl_b64 s[22:23], s[6:7], 23
	s_mov_b32 s25, s7
	s_add_u32 s26, s88, s22
	s_addc_u32 s27, s89, s23
	s_lshl_b64 s[22:23], s[24:25], 22
	s_add_u32 s22, s0, s22
	s_addc_u32 s23, s5, s23
	s_mov_b64 s[28:29], 0
